# GEMM K-loops: first K-iteration peeled with SrcC=0 so the 128-VGPR accumulator zeroing per output tile is gone (10 of 12 loops); plus the attention VALU trims of the previous version; bit-identical ou
# speedup vs baseline: 1.0189x; 1.0077x over previous
.LBB0_465:
	s_add_u32 s0, s50, 0x100
	s_addc_u32 s1, s51, 0
	s_mov_b32 s3, -2
.Lpeelg1_hdr:
	s_add_u32 s50, s42, 0x100
	s_addc_u32 s51, s43, 0
	s_cmp_eq_u32 s3, 12
	s_cselect_b32 s55, s49, s51
	s_cselect_b32 s54, s48, s50
	s_cselect_b32 s53, s47, s1
	s_cselect_b32 s52, s46, s0
	s_add_i32 s6, 0, 0x10400
	v_add_u32_e32 v2, s6, v155
	ds_read_b128 v[134:137], v2
	ds_read_b128 v[138:141], v2 offset:1024
	ds_read_b128 v[160:163], v2 offset:2048
	ds_read_b128 v[166:169], v2 offset:3072
	v_lshl_add_u64 v[182:183], s[42:43], 0, v[158:159]
	s_add_i32 m0, s59, 0xc400
	ds_read_b128 v[170:173], v164 offset:1024
	ds_read_b128 v[174:177], v164 offset:2048
	ds_read_b128 v[178:181], v164 offset:3072
	ds_read_b128 v[184:187], v164 offset:4096
	ds_read_b128 v[188:191], v164 offset:5120
	ds_read_b128 v[192:195], v164 offset:6144
	ds_read_b128 v[196:199], v164 offset:7168
	ds_read_b128 v[200:203], v164 offset:8192
	global_load_lds_dwordx4 v[182:183], off
	v_lshl_add_u64 v[182:183], s[42:43], 0, v[156:157]
	s_add_i32 m0, s59, 0xe400
	s_nop 0
	global_load_lds_dwordx4 v[182:183], off
	s_waitcnt lgkmcnt(8)
	s_barrier
	s_waitcnt lgkmcnt(0)
	s_setprio 1
	s_waitcnt lgkmcnt(0)
	v_mfma_f32_16x16x32_bf16 v[130:133], v[134:137], v[170:173], 0
	v_mfma_f32_16x16x32_bf16 v[126:129], v[160:163], v[170:173], 0
	v_mfma_f32_16x16x32_bf16 v[122:125], v[134:137], v[178:181], 0
	v_mfma_f32_16x16x32_bf16 v[118:121], v[160:163], v[178:181], 0
	v_mfma_f32_16x16x32_bf16 v[104:107], v[134:137], v[188:191], 0
	v_mfma_f32_16x16x32_bf16 v[100:103], v[160:163], v[188:191], 0
	v_mfma_f32_16x16x32_bf16 v[88:91], v[134:137], v[196:199], 0
	v_mfma_f32_16x16x32_bf16 v[84:87], v[160:163], v[196:199], 0
	v_mfma_f32_16x16x32_bf16 v[130:133], v[138:141], v[174:177], v[130:133]
	v_mfma_f32_16x16x32_bf16 v[126:129], v[166:169], v[174:177], v[126:129]
	v_mfma_f32_16x16x32_bf16 v[122:125], v[138:141], v[184:187], v[122:125]
	v_mfma_f32_16x16x32_bf16 v[118:121], v[166:169], v[184:187], v[118:121]
	v_mfma_f32_16x16x32_bf16 v[104:107], v[138:141], v[192:195], v[104:107]
	v_mfma_f32_16x16x32_bf16 v[100:103], v[166:169], v[192:195], v[100:103]
	v_mfma_f32_16x16x32_bf16 v[88:91], v[138:141], v[200:203], v[88:91]
	v_mfma_f32_16x16x32_bf16 v[84:87], v[166:169], v[200:203], v[84:87]
	s_setprio 0
	s_barrier
	s_add_i32 s37, 0, 0x14400
	s_add_i32 s6, s6, s58
	v_add_u32_e32 v2, s37, v155
	v_lshl_add_u64 v[182:183], s[52:53], 0, v[142:143]
	s_mov_b32 m0, s6
	ds_read_b128 v[204:207], v2
	ds_read_b128 v[208:211], v2 offset:1024
	ds_read_b128 v[212:215], v2 offset:2048
	ds_read_b128 v[216:219], v2 offset:3072
	global_load_lds_dwordx4 v[182:183], off
	v_lshl_add_u64 v[220:221], s[52:53], 0, v[144:145]
	s_add_i32 m0, s6, 0x2000
	s_nop 0
	global_load_lds_dwordx4 v[220:221], off
	s_barrier
	s_waitcnt lgkmcnt(0)
	s_setprio 1
	s_waitcnt lgkmcnt(0)
	v_mfma_f32_16x16x32_bf16 v[112:115], v[204:207], v[170:173], 0
	v_mfma_f32_16x16x32_bf16 v[108:111], v[212:215], v[170:173], 0
	v_mfma_f32_16x16x32_bf16 v[96:99], v[204:207], v[178:181], 0
	v_mfma_f32_16x16x32_bf16 v[92:95], v[212:215], v[178:181], 0
	v_mfma_f32_16x16x32_bf16 v[80:83], v[204:207], v[188:191], 0
	v_mfma_f32_16x16x32_bf16 v[76:79], v[212:215], v[188:191], 0
	v_mfma_f32_16x16x32_bf16 v[72:75], v[204:207], v[196:199], 0
	v_mfma_f32_16x16x32_bf16 v[64:67], v[212:215], v[196:199], 0
	v_mfma_f32_16x16x32_bf16 v[112:115], v[208:211], v[174:177], v[112:115]
	v_mfma_f32_16x16x32_bf16 v[108:111], v[216:219], v[174:177], v[108:111]
	v_mfma_f32_16x16x32_bf16 v[96:99], v[208:211], v[184:187], v[96:99]
	v_mfma_f32_16x16x32_bf16 v[92:95], v[216:219], v[184:187], v[92:95]
	v_mfma_f32_16x16x32_bf16 v[80:83], v[208:211], v[192:195], v[80:83]
	v_mfma_f32_16x16x32_bf16 v[76:79], v[216:219], v[192:195], v[76:79]
	v_mfma_f32_16x16x32_bf16 v[72:75], v[208:211], v[200:203], v[72:75]
	v_mfma_f32_16x16x32_bf16 v[64:67], v[216:219], v[200:203], v[64:67]
	s_setprio 0
	s_mov_b32 m0, s60
	v_lshl_add_u64 v[222:223], s[54:55], 0, v[146:147]
	s_barrier
	ds_read_b128 v[170:173], v164 offset:17408
	ds_read_b128 v[174:177], v164 offset:18432
	ds_read_b128 v[178:181], v164 offset:19456
	ds_read_b128 v[184:187], v164 offset:20480
	ds_read_b128 v[188:191], v164 offset:21504
	ds_read_b128 v[192:195], v164 offset:22528
	ds_read_b128 v[196:199], v164 offset:23552
	ds_read_b128 v[200:203], v164 offset:24576
	global_load_lds_dwordx4 v[222:223], off
	v_lshl_add_u64 v[224:225], s[54:55], 0, v[148:149]
	s_mov_b32 m0, s61
	s_nop 0
	global_load_lds_dwordx4 v[224:225], off
	s_barrier
	s_waitcnt lgkmcnt(0)
	s_setprio 1
	s_waitcnt lgkmcnt(0)
	v_mfma_f32_16x16x32_bf16 v[56:59], v[134:137], v[170:173], 0
	v_mfma_f32_16x16x32_bf16 v[48:51], v[160:163], v[170:173], 0
	v_mfma_f32_16x16x32_bf16 v[40:43], v[134:137], v[178:181], 0
	v_mfma_f32_16x16x32_bf16 v[36:39], v[160:163], v[178:181], 0
	v_mfma_f32_16x16x32_bf16 v[24:27], v[134:137], v[188:191], 0
	v_mfma_f32_16x16x32_bf16 v[20:23], v[160:163], v[188:191], 0
	v_mfma_f32_16x16x32_bf16 v[8:11], v[134:137], v[196:199], 0
	v_mfma_f32_16x16x32_bf16 v[4:7], v[160:163], v[196:199], 0
	v_mfma_f32_16x16x32_bf16 v[56:59], v[138:141], v[174:177], v[56:59]
	v_mfma_f32_16x16x32_bf16 v[48:51], v[166:169], v[174:177], v[48:51]
	v_mfma_f32_16x16x32_bf16 v[40:43], v[138:141], v[184:187], v[40:43]
	v_mfma_f32_16x16x32_bf16 v[36:39], v[166:169], v[184:187], v[36:39]
	v_mfma_f32_16x16x32_bf16 v[24:27], v[138:141], v[192:195], v[24:27]
	v_mfma_f32_16x16x32_bf16 v[20:23], v[166:169], v[192:195], v[20:23]
	v_mfma_f32_16x16x32_bf16 v[8:11], v[138:141], v[200:203], v[8:11]
	v_mfma_f32_16x16x32_bf16 v[4:7], v[166:169], v[200:203], v[4:7]
	s_setprio 0
	s_barrier
	s_add_u32 s42, s52, 0x40000
	s_addc_u32 s43, s53, 0
	s_add_i32 s6, s37, s58
	v_lshl_add_u64 v[134:135], s[42:43], 0, v[142:143]
	s_mov_b32 m0, s6
	s_nop 0
	global_load_lds_dwordx4 v[134:135], off
	v_lshl_add_u64 v[134:135], s[42:43], 0, v[144:145]
	s_add_i32 m0, s6, 0x2000
	s_nop 0
	global_load_lds_dwordx4 v[134:135], off
	s_waitcnt vmcnt(6)
	s_barrier
	s_setprio 1
	v_mfma_f32_16x16x32_bf16 v[32:35], v[204:207], v[170:173], 0
	v_mfma_f32_16x16x32_bf16 v[28:31], v[212:215], v[170:173], 0
	v_mfma_f32_16x16x32_bf16 v[16:19], v[204:207], v[178:181], 0
	v_mfma_f32_16x16x32_bf16 v[12:15], v[212:215], v[178:181], 0
	v_mfma_f32_16x16x32_bf16 v[60:63], v[204:207], v[188:191], 0
	v_mfma_f32_16x16x32_bf16 v[68:71], v[212:215], v[188:191], 0
	v_mfma_f32_16x16x32_bf16 v[44:47], v[204:207], v[196:199], 0
	v_mfma_f32_16x16x32_bf16 v[52:55], v[212:215], v[196:199], 0
	v_mfma_f32_16x16x32_bf16 v[32:35], v[208:211], v[174:177], v[32:35]
	v_mfma_f32_16x16x32_bf16 v[28:31], v[216:219], v[174:177], v[28:31]
	v_mfma_f32_16x16x32_bf16 v[16:19], v[208:211], v[184:187], v[16:19]
	v_mfma_f32_16x16x32_bf16 v[12:15], v[216:219], v[184:187], v[12:15]
	v_mfma_f32_16x16x32_bf16 v[60:63], v[208:211], v[192:195], v[60:63]
	v_mfma_f32_16x16x32_bf16 v[68:71], v[216:219], v[192:195], v[68:71]
	v_mfma_f32_16x16x32_bf16 v[44:47], v[208:211], v[200:203], v[44:47]
	v_mfma_f32_16x16x32_bf16 v[52:55], v[216:219], v[200:203], v[52:55]
	s_setprio 0
	s_add_i32 s6, 0, 0x18400
	v_add_u32_e32 v2, s6, v155
	s_barrier
	ds_read_b128 v[134:137], v2
	ds_read_b128 v[138:141], v2 offset:1024
	ds_read_b128 v[160:163], v2 offset:2048
	ds_read_b128 v[166:169], v2 offset:3072
	s_mov_b32 m0, s63
	v_lshl_add_u64 v[204:205], s[54:55], 0, v[150:151]
	ds_read_b128 v[170:173], v164 offset:33792
	ds_read_b128 v[174:177], v164 offset:34816
	ds_read_b128 v[178:181], v164 offset:35840
	ds_read_b128 v[184:187], v164 offset:36864
	ds_read_b128 v[188:191], v164 offset:37888
	ds_read_b128 v[192:195], v164 offset:38912
	ds_read_b128 v[196:199], v164 offset:39936
	ds_read_b128 v[200:203], v164 offset:40960
	global_load_lds_dwordx4 v[204:205], off
	v_lshl_add_u64 v[204:205], s[54:55], 0, v[152:153]
	s_mov_b32 m0, s64
	s_nop 0
	global_load_lds_dwordx4 v[204:205], off
	s_waitcnt lgkmcnt(8)
	s_barrier
	s_waitcnt lgkmcnt(0)
	s_setprio 1
	s_waitcnt lgkmcnt(0)
	v_mfma_f32_16x16x32_bf16 v[130:133], v[134:137], v[170:173], v[130:133]
	v_mfma_f32_16x16x32_bf16 v[126:129], v[160:163], v[170:173], v[126:129]
	v_mfma_f32_16x16x32_bf16 v[122:125], v[134:137], v[178:181], v[122:125]
	v_mfma_f32_16x16x32_bf16 v[118:121], v[160:163], v[178:181], v[118:121]
	v_mfma_f32_16x16x32_bf16 v[104:107], v[134:137], v[188:191], v[104:107]
	v_mfma_f32_16x16x32_bf16 v[100:103], v[160:163], v[188:191], v[100:103]
	v_mfma_f32_16x16x32_bf16 v[88:91], v[134:137], v[196:199], v[88:91]
	v_mfma_f32_16x16x32_bf16 v[84:87], v[160:163], v[196:199], v[84:87]
	v_mfma_f32_16x16x32_bf16 v[130:133], v[138:141], v[174:177], v[130:133]
	v_mfma_f32_16x16x32_bf16 v[126:129], v[166:169], v[174:177], v[126:129]
	v_mfma_f32_16x16x32_bf16 v[122:125], v[138:141], v[184:187], v[122:125]
	v_mfma_f32_16x16x32_bf16 v[118:121], v[166:169], v[184:187], v[118:121]
	v_mfma_f32_16x16x32_bf16 v[104:107], v[138:141], v[192:195], v[104:107]
	v_mfma_f32_16x16x32_bf16 v[100:103], v[166:169], v[192:195], v[100:103]
	v_mfma_f32_16x16x32_bf16 v[88:91], v[138:141], v[200:203], v[88:91]
	v_mfma_f32_16x16x32_bf16 v[84:87], v[166:169], v[200:203], v[84:87]
	s_setprio 0
	s_barrier
	s_add_i32 s37, 0, 0x1c400
	s_add_i32 s6, s6, s58
	v_add_u32_e32 v2, s37, v155
	v_lshl_add_u64 v[182:183], v[182:183], 0, s[22:23]
	s_mov_b32 m0, s6
	ds_read_b128 v[204:207], v2
	ds_read_b128 v[208:211], v2 offset:1024
	ds_read_b128 v[212:215], v2 offset:2048
	ds_read_b128 v[216:219], v2 offset:3072
	global_load_lds_dwordx4 v[182:183], off
	v_lshl_add_u64 v[182:183], v[220:221], 0, s[22:23]
	s_add_i32 m0, s6, 0x2000
	s_nop 0
	global_load_lds_dwordx4 v[182:183], off
	s_barrier
	s_waitcnt lgkmcnt(0)
	s_setprio 1
	s_waitcnt lgkmcnt(0)
	v_mfma_f32_16x16x32_bf16 v[112:115], v[204:207], v[170:173], v[112:115]
	v_mfma_f32_16x16x32_bf16 v[108:111], v[212:215], v[170:173], v[108:111]
	v_mfma_f32_16x16x32_bf16 v[96:99], v[204:207], v[178:181], v[96:99]
	v_mfma_f32_16x16x32_bf16 v[92:95], v[212:215], v[178:181], v[92:95]
	v_mfma_f32_16x16x32_bf16 v[80:83], v[204:207], v[188:191], v[80:83]
	v_mfma_f32_16x16x32_bf16 v[76:79], v[212:215], v[188:191], v[76:79]
	v_mfma_f32_16x16x32_bf16 v[72:75], v[204:207], v[196:199], v[72:75]
	v_mfma_f32_16x16x32_bf16 v[64:67], v[212:215], v[196:199], v[64:67]
	v_mfma_f32_16x16x32_bf16 v[112:115], v[208:211], v[174:177], v[112:115]
	v_mfma_f32_16x16x32_bf16 v[108:111], v[216:219], v[174:177], v[108:111]
	v_mfma_f32_16x16x32_bf16 v[96:99], v[208:211], v[184:187], v[96:99]
	v_mfma_f32_16x16x32_bf16 v[92:95], v[216:219], v[184:187], v[92:95]
	v_mfma_f32_16x16x32_bf16 v[80:83], v[208:211], v[192:195], v[80:83]
	v_mfma_f32_16x16x32_bf16 v[76:79], v[216:219], v[192:195], v[76:79]
	v_mfma_f32_16x16x32_bf16 v[72:75], v[208:211], v[200:203], v[72:75]
	v_mfma_f32_16x16x32_bf16 v[64:67], v[216:219], v[200:203], v[64:67]
	s_setprio 0
	s_mov_b32 m0, s68
	v_lshl_add_u64 v[182:183], v[222:223], 0, s[22:23]
	s_barrier
	ds_read_b128 v[170:173], v164 offset:50176
	ds_read_b128 v[174:177], v164 offset:51200
	ds_read_b128 v[178:181], v164 offset:52224
	ds_read_b128 v[184:187], v164 offset:53248
	ds_read_b128 v[188:191], v164 offset:54272
	ds_read_b128 v[192:195], v164 offset:55296
	ds_read_b128 v[196:199], v164 offset:56320
	ds_read_b128 v[200:203], v164 offset:57344
	global_load_lds_dwordx4 v[182:183], off
	v_lshl_add_u64 v[182:183], v[224:225], 0, s[22:23]
	s_mov_b32 m0, s69
	s_nop 0
	global_load_lds_dwordx4 v[182:183], off
	s_barrier
	s_waitcnt lgkmcnt(0)
	s_setprio 1
	s_waitcnt lgkmcnt(0)
	v_mfma_f32_16x16x32_bf16 v[56:59], v[134:137], v[170:173], v[56:59]
	v_mfma_f32_16x16x32_bf16 v[48:51], v[160:163], v[170:173], v[48:51]
	v_mfma_f32_16x16x32_bf16 v[40:43], v[134:137], v[178:181], v[40:43]
	v_mfma_f32_16x16x32_bf16 v[36:39], v[160:163], v[178:181], v[36:39]
	v_mfma_f32_16x16x32_bf16 v[24:27], v[134:137], v[188:191], v[24:27]
	v_mfma_f32_16x16x32_bf16 v[20:23], v[160:163], v[188:191], v[20:23]
	v_mfma_f32_16x16x32_bf16 v[8:11], v[134:137], v[196:199], v[8:11]
	v_mfma_f32_16x16x32_bf16 v[4:7], v[160:163], v[196:199], v[4:7]
	v_mfma_f32_16x16x32_bf16 v[56:59], v[138:141], v[174:177], v[56:59]
	v_mfma_f32_16x16x32_bf16 v[48:51], v[166:169], v[174:177], v[48:51]
	v_mfma_f32_16x16x32_bf16 v[40:43], v[138:141], v[184:187], v[40:43]
	v_mfma_f32_16x16x32_bf16 v[36:39], v[166:169], v[184:187], v[36:39]
	v_mfma_f32_16x16x32_bf16 v[24:27], v[138:141], v[192:195], v[24:27]
	v_mfma_f32_16x16x32_bf16 v[20:23], v[166:169], v[192:195], v[20:23]
	v_mfma_f32_16x16x32_bf16 v[8:11], v[138:141], v[200:203], v[8:11]
	v_mfma_f32_16x16x32_bf16 v[4:7], v[166:169], v[200:203], v[4:7]
	s_setprio 0
	s_barrier
	s_add_u32 s42, s52, 0x40080
	s_addc_u32 s43, s53, 0
	s_add_i32 s6, s37, s58
	v_lshl_add_u64 v[134:135], s[42:43], 0, v[142:143]
	s_mov_b32 m0, s6
	s_nop 0
	global_load_lds_dwordx4 v[134:135], off
	v_lshl_add_u64 v[134:135], s[42:43], 0, v[144:145]
	s_add_i32 m0, s6, 0x2000
	s_nop 0
	global_load_lds_dwordx4 v[134:135], off
	s_waitcnt vmcnt(6)
	s_barrier
	s_setprio 1
	v_mfma_f32_16x16x32_bf16 v[32:35], v[204:207], v[170:173], v[32:35]
	v_mfma_f32_16x16x32_bf16 v[28:31], v[212:215], v[170:173], v[28:31]
	v_mfma_f32_16x16x32_bf16 v[16:19], v[204:207], v[178:181], v[16:19]
	v_mfma_f32_16x16x32_bf16 v[12:15], v[212:215], v[178:181], v[12:15]
	v_mfma_f32_16x16x32_bf16 v[60:63], v[204:207], v[188:191], v[60:63]
	v_mfma_f32_16x16x32_bf16 v[68:71], v[212:215], v[188:191], v[68:71]
	v_mfma_f32_16x16x32_bf16 v[44:47], v[204:207], v[196:199], v[44:47]
	v_mfma_f32_16x16x32_bf16 v[52:55], v[212:215], v[196:199], v[52:55]
	v_mfma_f32_16x16x32_bf16 v[32:35], v[208:211], v[174:177], v[32:35]
	v_mfma_f32_16x16x32_bf16 v[28:31], v[216:219], v[174:177], v[28:31]
	v_mfma_f32_16x16x32_bf16 v[16:19], v[208:211], v[184:187], v[16:19]
	v_mfma_f32_16x16x32_bf16 v[12:15], v[216:219], v[184:187], v[12:15]
	v_mfma_f32_16x16x32_bf16 v[60:63], v[208:211], v[192:195], v[60:63]
	v_mfma_f32_16x16x32_bf16 v[68:71], v[216:219], v[192:195], v[68:71]
	v_mfma_f32_16x16x32_bf16 v[44:47], v[208:211], v[200:203], v[44:47]
	v_mfma_f32_16x16x32_bf16 v[52:55], v[216:219], v[200:203], v[52:55]
	s_setprio 0
	s_add_i32 s3, s3, 2
	s_add_u32 s0, s0, 0x100
	s_addc_u32 s1, s1, 0
	s_cmp_gt_u32 s3, 13
	s_mov_b64 s[42:43], s[50:51]
	s_barrier
	s_cbranch_scc0 .LBB0_466
	s_branch .Lpexit_g1

.Lpexit_g1:
	v_lshl_add_u32 v160, s40, 8, v117
	s_mov_b64 s[0:1], -1
	s_cmp_gt_i32 s65, 2
	v_ashrrev_i32_e32 v161, 31, v160
	s_cbranch_scc0 .LBB0_505
	s_cmp_eq_u32 s65, 5
	s_cselect_b64 s[42:43], -1, 0
	s_cmp_lg_u32 s65, 5
	s_cbranch_scc0 .LBB0_470
	v_lshlrev_b64 v[134:135], 9, v[160:161]
	s_cmp_eq_u32 s65, 4
	v_lshl_add_u64 v[134:135], s[8:9], 0, v[134:135]
	s_cselect_b32 s76, 0x100, 0
	v_lshl_add_u64 v[162:163], v[134:135], 0, s[76:77]
	s_mov_b64 s[0:1], 0

.LBB0_805:
	s_add_u32 s0, s50, 0x100
	s_addc_u32 s1, s51, 0
	s_add_u32 s50, s52, 0x80
	s_addc_u32 s51, s53, 0
	s_mov_b32 s71, -2
.Lpeelwo2_hdr:
	s_add_u32 s52, s50, 0x80
	s_addc_u32 s53, s51, 0
	s_cmp_eq_u32 s71, 12
	s_cselect_b32 s55, s47, s53
	s_cselect_b32 s54, s46, s52
	s_cselect_b32 s53, s49, s1
	s_cselect_b32 s52, s48, s0
	s_add_i32 s72, 0, 0x10400
	v_add_u32_e32 v146, s72, v172
	ds_read_b128 v[134:137], v146
	ds_read_b128 v[138:141], v146 offset:1024
	ds_read_b128 v[142:145], v146 offset:2048
	ds_read_b128 v[146:149], v146 offset:3072
	v_lshl_add_u64 v[180:181], s[50:51], 0, v[166:167]
	s_add_i32 m0, s59, 0xc400
	ds_read_b128 v[150:153], v174 offset:1024
	ds_read_b128 v[168:171], v174 offset:2048
	ds_read_b128 v[176:179], v174 offset:3072
	ds_read_b128 v[184:187], v174 offset:4096
	ds_read_b128 v[188:191], v174 offset:5120
	ds_read_b128 v[192:195], v174 offset:6144
	ds_read_b128 v[196:199], v174 offset:7168
	ds_read_b128 v[200:203], v174 offset:8192
	global_load_lds_dwordx4 v[180:181], off
	v_lshl_add_u64 v[180:181], s[50:51], 0, v[164:165]
	s_add_i32 m0, s59, 0xe400
	s_nop 0
	global_load_lds_dwordx4 v[180:181], off
	s_waitcnt lgkmcnt(8)
	s_barrier
	s_waitcnt lgkmcnt(0)
	s_setprio 1
	s_waitcnt lgkmcnt(0)
	v_mfma_f32_16x16x32_bf16 v[130:133], v[134:137], v[150:153], 0
	v_mfma_f32_16x16x32_bf16 v[126:129], v[142:145], v[150:153], 0
	v_mfma_f32_16x16x32_bf16 v[118:121], v[134:137], v[176:179], 0
	v_mfma_f32_16x16x32_bf16 v[108:111], v[142:145], v[176:179], 0
	v_mfma_f32_16x16x32_bf16 v[100:103], v[134:137], v[188:191], 0
	v_mfma_f32_16x16x32_bf16 v[92:95], v[142:145], v[188:191], 0
	v_mfma_f32_16x16x32_bf16 v[84:87], v[134:137], v[196:199], 0
	v_mfma_f32_16x16x32_bf16 v[76:79], v[142:145], v[196:199], 0
	v_mfma_f32_16x16x32_bf16 v[130:133], v[138:141], v[168:171], v[130:133]
	v_mfma_f32_16x16x32_bf16 v[126:129], v[146:149], v[168:171], v[126:129]
	v_mfma_f32_16x16x32_bf16 v[118:121], v[138:141], v[184:187], v[118:121]
	v_mfma_f32_16x16x32_bf16 v[108:111], v[146:149], v[184:187], v[108:111]
	v_mfma_f32_16x16x32_bf16 v[100:103], v[138:141], v[192:195], v[100:103]
	v_mfma_f32_16x16x32_bf16 v[92:95], v[146:149], v[192:195], v[92:95]
	v_mfma_f32_16x16x32_bf16 v[84:87], v[138:141], v[200:203], v[84:87]
	v_mfma_f32_16x16x32_bf16 v[76:79], v[146:149], v[200:203], v[76:79]
	s_setprio 0
	s_barrier
	s_add_i32 s74, 0, 0x14400
	s_add_i32 s72, s72, s56
	v_add_u32_e32 v175, s74, v172
	v_lshl_add_u64 v[180:181], s[52:53], 0, v[2:3]
	s_mov_b32 m0, s72
	ds_read_b128 v[204:207], v175
	ds_read_b128 v[208:211], v175 offset:1024
	ds_read_b128 v[212:215], v175 offset:2048
	ds_read_b128 v[216:219], v175 offset:3072
	global_load_lds_dwordx4 v[180:181], off
	v_lshl_add_u64 v[182:183], s[52:53], 0, v[154:155]
	s_add_i32 m0, s72, 0x2000
	s_nop 0
	global_load_lds_dwordx4 v[182:183], off
	s_barrier
	s_waitcnt lgkmcnt(0)
	s_setprio 1
	s_waitcnt lgkmcnt(0)
	v_mfma_f32_16x16x32_bf16 v[122:125], v[204:207], v[150:153], 0
	v_mfma_f32_16x16x32_bf16 v[112:115], v[212:215], v[150:153], 0
	v_mfma_f32_16x16x32_bf16 v[104:107], v[204:207], v[176:179], 0
	v_mfma_f32_16x16x32_bf16 v[96:99], v[212:215], v[176:179], 0
	v_mfma_f32_16x16x32_bf16 v[88:91], v[204:207], v[188:191], 0
	v_mfma_f32_16x16x32_bf16 v[80:83], v[212:215], v[188:191], 0
	v_mfma_f32_16x16x32_bf16 v[72:75], v[204:207], v[196:199], 0
	v_mfma_f32_16x16x32_bf16 v[68:71], v[212:215], v[196:199], 0
	v_mfma_f32_16x16x32_bf16 v[122:125], v[208:211], v[168:171], v[122:125]
	v_mfma_f32_16x16x32_bf16 v[112:115], v[216:219], v[168:171], v[112:115]
	v_mfma_f32_16x16x32_bf16 v[104:107], v[208:211], v[184:187], v[104:107]
	v_mfma_f32_16x16x32_bf16 v[96:99], v[216:219], v[184:187], v[96:99]
	v_mfma_f32_16x16x32_bf16 v[88:91], v[208:211], v[192:195], v[88:91]
	v_mfma_f32_16x16x32_bf16 v[80:83], v[216:219], v[192:195], v[80:83]
	v_mfma_f32_16x16x32_bf16 v[72:75], v[208:211], v[200:203], v[72:75]
	v_mfma_f32_16x16x32_bf16 v[68:71], v[216:219], v[200:203], v[68:71]
	s_setprio 0
	s_mov_b32 m0, s60
	v_lshl_add_u64 v[220:221], s[54:55], 0, v[156:157]
	s_barrier
	ds_read_b128 v[150:153], v174 offset:17408
	ds_read_b128 v[168:171], v174 offset:18432
	ds_read_b128 v[176:179], v174 offset:19456
	ds_read_b128 v[184:187], v174 offset:20480
	ds_read_b128 v[188:191], v174 offset:21504
	ds_read_b128 v[192:195], v174 offset:22528
	ds_read_b128 v[196:199], v174 offset:23552
	ds_read_b128 v[200:203], v174 offset:24576
	global_load_lds_dwordx4 v[220:221], off
	v_lshl_add_u64 v[222:223], s[54:55], 0, v[158:159]
	s_mov_b32 m0, s61
	s_nop 0
	global_load_lds_dwordx4 v[222:223], off
	s_barrier
	s_waitcnt lgkmcnt(0)
	s_setprio 1
	s_waitcnt lgkmcnt(0)
	v_mfma_f32_16x16x32_bf16 v[64:67], v[134:137], v[150:153], 0
	v_mfma_f32_16x16x32_bf16 v[60:63], v[142:145], v[150:153], 0
	v_mfma_f32_16x16x32_bf16 v[52:55], v[134:137], v[176:179], 0
	v_mfma_f32_16x16x32_bf16 v[44:47], v[142:145], v[176:179], 0
	v_mfma_f32_16x16x32_bf16 v[28:31], v[134:137], v[188:191], 0
	v_mfma_f32_16x16x32_bf16 v[12:15], v[142:145], v[188:191], 0
	v_mfma_f32_16x16x32_bf16 v[8:11], v[134:137], v[196:199], 0
	v_mfma_f32_16x16x32_bf16 v[4:7], v[142:145], v[196:199], 0
	v_mfma_f32_16x16x32_bf16 v[64:67], v[138:141], v[168:171], v[64:67]
	v_mfma_f32_16x16x32_bf16 v[60:63], v[146:149], v[168:171], v[60:63]
	v_mfma_f32_16x16x32_bf16 v[52:55], v[138:141], v[184:187], v[52:55]
	v_mfma_f32_16x16x32_bf16 v[44:47], v[146:149], v[184:187], v[44:47]
	v_mfma_f32_16x16x32_bf16 v[28:31], v[138:141], v[192:195], v[28:31]
	v_mfma_f32_16x16x32_bf16 v[12:15], v[146:149], v[192:195], v[12:15]
	v_mfma_f32_16x16x32_bf16 v[8:11], v[138:141], v[200:203], v[8:11]
	v_mfma_f32_16x16x32_bf16 v[4:7], v[146:149], v[200:203], v[4:7]
	s_setprio 0
	s_barrier
	s_add_u32 s72, s52, 0x40000
	s_addc_u32 s73, s53, 0
	s_add_i32 s74, s74, s56
	v_lshl_add_u64 v[134:135], s[72:73], 0, v[2:3]
	s_mov_b32 m0, s74
	s_nop 0
	global_load_lds_dwordx4 v[134:135], off
	v_lshl_add_u64 v[134:135], s[72:73], 0, v[154:155]
	s_add_i32 m0, s74, 0x2000
	s_nop 0
	global_load_lds_dwordx4 v[134:135], off
	s_waitcnt vmcnt(6)
	s_barrier
	s_setprio 1
	v_mfma_f32_16x16x32_bf16 v[56:59], v[204:207], v[150:153], 0
	v_mfma_f32_16x16x32_bf16 v[48:51], v[212:215], v[150:153], 0
	v_mfma_f32_16x16x32_bf16 v[32:35], v[204:207], v[176:179], 0
	v_mfma_f32_16x16x32_bf16 v[20:23], v[212:215], v[176:179], 0
	v_mfma_f32_16x16x32_bf16 v[40:43], v[204:207], v[188:191], 0
	v_mfma_f32_16x16x32_bf16 v[36:39], v[212:215], v[188:191], 0
	v_mfma_f32_16x16x32_bf16 v[24:27], v[204:207], v[196:199], 0
	v_mfma_f32_16x16x32_bf16 v[16:19], v[212:215], v[196:199], 0
	v_mfma_f32_16x16x32_bf16 v[56:59], v[208:211], v[168:171], v[56:59]
	v_mfma_f32_16x16x32_bf16 v[48:51], v[216:219], v[168:171], v[48:51]
	v_mfma_f32_16x16x32_bf16 v[32:35], v[208:211], v[184:187], v[32:35]
	v_mfma_f32_16x16x32_bf16 v[20:23], v[216:219], v[184:187], v[20:23]
	v_mfma_f32_16x16x32_bf16 v[40:43], v[208:211], v[192:195], v[40:43]
	v_mfma_f32_16x16x32_bf16 v[36:39], v[216:219], v[192:195], v[36:39]
	v_mfma_f32_16x16x32_bf16 v[24:27], v[208:211], v[200:203], v[24:27]
	v_mfma_f32_16x16x32_bf16 v[16:19], v[216:219], v[200:203], v[16:19]
	s_setprio 0
	s_add_i32 s72, 0, 0x18400
	v_add_u32_e32 v146, s72, v172
	s_barrier
	ds_read_b128 v[134:137], v146
	ds_read_b128 v[138:141], v146 offset:1024
	ds_read_b128 v[142:145], v146 offset:2048
	ds_read_b128 v[146:149], v146 offset:3072
	s_mov_b32 m0, s62
	v_lshl_add_u64 v[204:205], s[54:55], 0, v[160:161]
	ds_read_b128 v[150:153], v174 offset:33792
	ds_read_b128 v[168:171], v174 offset:34816
	ds_read_b128 v[176:179], v174 offset:35840
	ds_read_b128 v[184:187], v174 offset:36864
	ds_read_b128 v[188:191], v174 offset:37888
	ds_read_b128 v[192:195], v174 offset:38912
	ds_read_b128 v[196:199], v174 offset:39936
	ds_read_b128 v[200:203], v174 offset:40960
	global_load_lds_dwordx4 v[204:205], off
	v_lshl_add_u64 v[204:205], s[54:55], 0, v[162:163]
	s_mov_b32 m0, s63
	s_nop 0
	global_load_lds_dwordx4 v[204:205], off
	s_waitcnt lgkmcnt(8)
	s_barrier
	s_waitcnt lgkmcnt(0)
	s_setprio 1
	s_waitcnt lgkmcnt(0)
	v_mfma_f32_16x16x32_bf16 v[130:133], v[134:137], v[150:153], v[130:133]
	v_mfma_f32_16x16x32_bf16 v[126:129], v[142:145], v[150:153], v[126:129]
	v_mfma_f32_16x16x32_bf16 v[118:121], v[134:137], v[176:179], v[118:121]
	v_mfma_f32_16x16x32_bf16 v[108:111], v[142:145], v[176:179], v[108:111]
	v_mfma_f32_16x16x32_bf16 v[100:103], v[134:137], v[188:191], v[100:103]
	v_mfma_f32_16x16x32_bf16 v[92:95], v[142:145], v[188:191], v[92:95]
	v_mfma_f32_16x16x32_bf16 v[84:87], v[134:137], v[196:199], v[84:87]
	v_mfma_f32_16x16x32_bf16 v[76:79], v[142:145], v[196:199], v[76:79]
	v_mfma_f32_16x16x32_bf16 v[130:133], v[138:141], v[168:171], v[130:133]
	v_mfma_f32_16x16x32_bf16 v[126:129], v[146:149], v[168:171], v[126:129]
	v_mfma_f32_16x16x32_bf16 v[118:121], v[138:141], v[184:187], v[118:121]
	v_mfma_f32_16x16x32_bf16 v[108:111], v[146:149], v[184:187], v[108:111]
	v_mfma_f32_16x16x32_bf16 v[100:103], v[138:141], v[192:195], v[100:103]
	v_mfma_f32_16x16x32_bf16 v[92:95], v[146:149], v[192:195], v[92:95]
	v_mfma_f32_16x16x32_bf16 v[84:87], v[138:141], v[200:203], v[84:87]
	v_mfma_f32_16x16x32_bf16 v[76:79], v[146:149], v[200:203], v[76:79]
	s_setprio 0
	s_barrier
	s_add_i32 s54, 0, 0x1c400
	s_add_i32 s55, s72, s56
	v_add_u32_e32 v175, s54, v172
	v_lshl_add_u64 v[180:181], v[180:181], 0, s[22:23]
	s_mov_b32 m0, s55
	ds_read_b128 v[204:207], v175
	ds_read_b128 v[208:211], v175 offset:1024
	ds_read_b128 v[212:215], v175 offset:2048
	ds_read_b128 v[216:219], v175 offset:3072
	global_load_lds_dwordx4 v[180:181], off
	v_lshl_add_u64 v[180:181], v[182:183], 0, s[22:23]
	s_add_i32 m0, s55, 0x2000
	s_nop 0
	global_load_lds_dwordx4 v[180:181], off
	s_barrier
	s_waitcnt lgkmcnt(0)
	s_setprio 1
	s_waitcnt lgkmcnt(0)
	v_mfma_f32_16x16x32_bf16 v[122:125], v[204:207], v[150:153], v[122:125]
	v_mfma_f32_16x16x32_bf16 v[112:115], v[212:215], v[150:153], v[112:115]
	v_mfma_f32_16x16x32_bf16 v[104:107], v[204:207], v[176:179], v[104:107]
	v_mfma_f32_16x16x32_bf16 v[96:99], v[212:215], v[176:179], v[96:99]
	v_mfma_f32_16x16x32_bf16 v[88:91], v[204:207], v[188:191], v[88:91]
	v_mfma_f32_16x16x32_bf16 v[80:83], v[212:215], v[188:191], v[80:83]
	v_mfma_f32_16x16x32_bf16 v[72:75], v[204:207], v[196:199], v[72:75]
	v_mfma_f32_16x16x32_bf16 v[68:71], v[212:215], v[196:199], v[68:71]
	v_mfma_f32_16x16x32_bf16 v[122:125], v[208:211], v[168:171], v[122:125]
	v_mfma_f32_16x16x32_bf16 v[112:115], v[216:219], v[168:171], v[112:115]
	v_mfma_f32_16x16x32_bf16 v[104:107], v[208:211], v[184:187], v[104:107]
	v_mfma_f32_16x16x32_bf16 v[96:99], v[216:219], v[184:187], v[96:99]
	v_mfma_f32_16x16x32_bf16 v[88:91], v[208:211], v[192:195], v[88:91]
	v_mfma_f32_16x16x32_bf16 v[80:83], v[216:219], v[192:195], v[80:83]
	v_mfma_f32_16x16x32_bf16 v[72:75], v[208:211], v[200:203], v[72:75]
	v_mfma_f32_16x16x32_bf16 v[68:71], v[216:219], v[200:203], v[68:71]
	s_setprio 0
	s_mov_b32 m0, s64
	v_lshl_add_u64 v[180:181], v[220:221], 0, s[22:23]
	s_barrier
	ds_read_b128 v[150:153], v174 offset:50176
	ds_read_b128 v[168:171], v174 offset:51200
	ds_read_b128 v[176:179], v174 offset:52224
	ds_read_b128 v[184:187], v174 offset:53248
	ds_read_b128 v[188:191], v174 offset:54272
	ds_read_b128 v[192:195], v174 offset:55296
	ds_read_b128 v[196:199], v174 offset:56320
	ds_read_b128 v[200:203], v174 offset:57344
	global_load_lds_dwordx4 v[180:181], off
	v_lshl_add_u64 v[180:181], v[222:223], 0, s[22:23]
	s_mov_b32 m0, s65
	s_nop 0
	global_load_lds_dwordx4 v[180:181], off
	s_barrier
	s_waitcnt lgkmcnt(0)
	s_setprio 1
	s_waitcnt lgkmcnt(0)
	v_mfma_f32_16x16x32_bf16 v[64:67], v[134:137], v[150:153], v[64:67]
	v_mfma_f32_16x16x32_bf16 v[60:63], v[142:145], v[150:153], v[60:63]
	v_mfma_f32_16x16x32_bf16 v[52:55], v[134:137], v[176:179], v[52:55]
	v_mfma_f32_16x16x32_bf16 v[44:47], v[142:145], v[176:179], v[44:47]
	v_mfma_f32_16x16x32_bf16 v[28:31], v[134:137], v[188:191], v[28:31]
	v_mfma_f32_16x16x32_bf16 v[12:15], v[142:145], v[188:191], v[12:15]
	v_mfma_f32_16x16x32_bf16 v[8:11], v[134:137], v[196:199], v[8:11]
	v_mfma_f32_16x16x32_bf16 v[4:7], v[142:145], v[196:199], v[4:7]
	v_mfma_f32_16x16x32_bf16 v[64:67], v[138:141], v[168:171], v[64:67]
	v_mfma_f32_16x16x32_bf16 v[60:63], v[146:149], v[168:171], v[60:63]
	v_mfma_f32_16x16x32_bf16 v[52:55], v[138:141], v[184:187], v[52:55]
	v_mfma_f32_16x16x32_bf16 v[44:47], v[146:149], v[184:187], v[44:47]
	v_mfma_f32_16x16x32_bf16 v[28:31], v[138:141], v[192:195], v[28:31]
	v_mfma_f32_16x16x32_bf16 v[12:15], v[146:149], v[192:195], v[12:15]
	v_mfma_f32_16x16x32_bf16 v[8:11], v[138:141], v[200:203], v[8:11]
	v_mfma_f32_16x16x32_bf16 v[4:7], v[146:149], v[200:203], v[4:7]
	s_setprio 0
	s_barrier
	s_add_u32 s52, s52, 0x40080
	s_addc_u32 s53, s53, 0
	s_add_i32 s54, s54, s56
	v_lshl_add_u64 v[134:135], s[52:53], 0, v[2:3]
	s_mov_b32 m0, s54
	s_nop 0
	global_load_lds_dwordx4 v[134:135], off
	v_lshl_add_u64 v[134:135], s[52:53], 0, v[154:155]
	s_add_i32 m0, s54, 0x2000
	s_nop 0
	global_load_lds_dwordx4 v[134:135], off
	s_waitcnt vmcnt(6)
	s_barrier
	s_setprio 1
	v_mfma_f32_16x16x32_bf16 v[56:59], v[204:207], v[150:153], v[56:59]
	v_mfma_f32_16x16x32_bf16 v[48:51], v[212:215], v[150:153], v[48:51]
	v_mfma_f32_16x16x32_bf16 v[32:35], v[204:207], v[176:179], v[32:35]
	v_mfma_f32_16x16x32_bf16 v[20:23], v[212:215], v[176:179], v[20:23]
	v_mfma_f32_16x16x32_bf16 v[40:43], v[204:207], v[188:191], v[40:43]
	v_mfma_f32_16x16x32_bf16 v[36:39], v[212:215], v[188:191], v[36:39]
	v_mfma_f32_16x16x32_bf16 v[24:27], v[204:207], v[196:199], v[24:27]
	v_mfma_f32_16x16x32_bf16 v[16:19], v[212:215], v[196:199], v[16:19]
	v_mfma_f32_16x16x32_bf16 v[56:59], v[208:211], v[168:171], v[56:59]
	v_mfma_f32_16x16x32_bf16 v[48:51], v[216:219], v[168:171], v[48:51]
	v_mfma_f32_16x16x32_bf16 v[32:35], v[208:211], v[184:187], v[32:35]
	v_mfma_f32_16x16x32_bf16 v[20:23], v[216:219], v[184:187], v[20:23]
	v_mfma_f32_16x16x32_bf16 v[40:43], v[208:211], v[192:195], v[40:43]
	v_mfma_f32_16x16x32_bf16 v[36:39], v[216:219], v[192:195], v[36:39]
	v_mfma_f32_16x16x32_bf16 v[24:27], v[208:211], v[200:203], v[24:27]
	v_mfma_f32_16x16x32_bf16 v[16:19], v[216:219], v[200:203], v[16:19]
	s_setprio 0
	s_add_i32 s71, s71, 2
	s_add_u32 s0, s0, 0x100
	s_addc_u32 s1, s1, 0
	s_add_u32 s50, s50, 0x100
	s_addc_u32 s51, s51, 0
	s_cmp_gt_u32 s71, 13
	s_barrier
	s_cbranch_scc0 .LBB0_806
	s_branch .Lpexit_wo2

.Lpexit_wo2:
	s_lshl_b32 s0, s69, 8
	v_add_u32_e32 v152, s0, v117
	v_ashrrev_i32_e32 v153, 31, v152
	v_lshl_or_b32 v150, s70, 8, v173
	v_lshlrev_b64 v[152:153], 11, v[152:153]
	v_ashrrev_i32_e32 v151, 31, v150
	v_lshl_add_u64 v[152:153], s[36:37], 0, v[152:153]
	s_min_i32 s1, s0, 0x8000
	v_lshl_add_u64 v[168:169], v[150:151], 1, v[152:153]
	s_ashr_i32 s1, s1, 12
	v_add_co_u32_e32 v180, vcc, s31, v168
	v_mul_hi_i32_i24_e32 v135, s1, v253
	v_mul_i32_i24_e32 v134, s1, v253
	v_addc_co_u32_e32 v181, vcc, 0, v169, vcc
	s_mov_b32 s0, 0x10000
	v_lshl_add_u64 v[134:135], s[44:45], 0, v[134:135]
	v_add_co_u32_e32 v182, vcc, s0, v168
	v_lshl_add_u64 v[138:139], v[150:151], 2, v[134:135]
	s_nop 0
	v_addc_co_u32_e32 v183, vcc, 0, v169, vcc
	s_mov_b32 s0, 0x18000
	global_load_dwordx4 v[142:145], v[138:139], off offset:16
	global_load_dwordx4 v[146:149], v[138:139], off
	global_load_dwordx4 v[134:137], v[138:139], off offset:528
	s_nop 0
	global_load_dwordx4 v[138:141], v[138:139], off offset:512
	v_add_co_u32_e32 v170, vcc, s0, v168
	global_load_dwordx4 v[176:179], v[168:169], off
	global_load_dwordx4 v[184:187], v[168:169], off offset:256
	v_addc_co_u32_e32 v171, vcc, 0, v169, vcc
	global_load_dwordx4 v[188:191], v[180:181], off
	global_load_dwordx4 v[192:195], v[180:181], off offset:256
	global_load_dwordx4 v[196:199], v[182:183], off
	global_load_dwordx4 v[200:203], v[182:183], off offset:256
	global_load_dwordx4 v[204:207], v[170:171], off
	global_load_dwordx4 v[150:153], v[170:171], off offset:256
	s_waitcnt vmcnt(0)
	v_lshlrev_b32_e32 v208, 16, v176
	v_and_b32_e32 v209, 0xffff0000, v176
	v_lshlrev_b32_e32 v176, 16, v177
	v_and_b32_e32 v177, 0xffff0000, v177
	v_pk_fma_f32 v[132:133], v[132:133], v[148:149], v[176:177]
	v_lshlrev_b32_e32 v176, 16, v178
	v_and_b32_e32 v177, 0xffff0000, v178
	v_lshlrev_b32_e32 v178, 16, v179
	v_and_b32_e32 v179, 0xffff0000, v179
	v_pk_fma_f32 v[130:131], v[130:131], v[146:147], v[208:209]
	v_pk_fma_f32 v[178:179], v[128:129], v[144:145], v[178:179]
	v_pk_fma_f32 v[128:129], v[126:127], v[142:143], v[176:177]
	v_cvt_pk_bf16_f32 v126, v130, v131
	v_cvt_pk_bf16_f32 v127, v132, v133
	v_cvt_pk_bf16_f32 v128, v128, v129
	v_cvt_pk_bf16_f32 v129, v178, v179
	global_store_dwordx4 v[168:169], v[126:129], off
	s_nop 1
	v_lshlrev_b32_e32 v126, 16, v184
	v_and_b32_e32 v127, 0xffff0000, v184
	v_lshlrev_b32_e32 v128, 16, v185
	v_and_b32_e32 v129, 0xffff0000, v185
	v_pk_fma_f32 v[124:125], v[124:125], v[140:141], v[128:129]
	v_pk_fma_f32 v[122:123], v[122:123], v[138:139], v[126:127]
	v_lshlrev_b32_e32 v126, 16, v186
	v_and_b32_e32 v127, 0xffff0000, v186
	v_lshlrev_b32_e32 v128, 16, v187
	v_and_b32_e32 v129, 0xffff0000, v187
	v_pk_fma_f32 v[128:129], v[114:115], v[136:137], v[128:129]
	v_pk_fma_f32 v[114:115], v[112:113], v[134:135], v[126:127]
	v_cvt_pk_bf16_f32 v112, v122, v123
	v_cvt_pk_bf16_f32 v113, v124, v125
	v_cvt_pk_bf16_f32 v114, v114, v115
	v_cvt_pk_bf16_f32 v115, v128, v129
	global_store_dwordx4 v[168:169], v[112:115], off offset:256
	s_nop 1
	v_lshlrev_b32_e32 v112, 16, v188
	v_and_b32_e32 v113, 0xffff0000, v188
	v_lshlrev_b32_e32 v114, 16, v189
	v_and_b32_e32 v115, 0xffff0000, v189
	v_pk_fma_f32 v[114:115], v[120:121], v[148:149], v[114:115]
	v_pk_fma_f32 v[112:113], v[118:119], v[146:147], v[112:113]
	v_lshlrev_b32_e32 v118, 16, v190
	v_and_b32_e32 v119, 0xffff0000, v190
	v_lshlrev_b32_e32 v120, 16, v191
	v_and_b32_e32 v121, 0xffff0000, v191
	v_pk_fma_f32 v[120:121], v[110:111], v[144:145], v[120:121]
	v_pk_fma_f32 v[110:111], v[108:109], v[142:143], v[118:119]
	v_cvt_pk_bf16_f32 v108, v112, v113
	v_cvt_pk_bf16_f32 v109, v114, v115
	v_cvt_pk_bf16_f32 v110, v110, v111
	v_cvt_pk_bf16_f32 v111, v120, v121
	global_store_dwordx4 v[180:181], v[108:111], off
	s_nop 1
	v_lshlrev_b32_e32 v108, 16, v192
	v_and_b32_e32 v109, 0xffff0000, v192
	v_lshlrev_b32_e32 v110, 16, v193
	v_and_b32_e32 v111, 0xffff0000, v193
	v_pk_fma_f32 v[106:107], v[106:107], v[140:141], v[110:111]
	v_pk_fma_f32 v[104:105], v[104:105], v[138:139], v[108:109]
	v_lshlrev_b32_e32 v108, 16, v194
	v_and_b32_e32 v109, 0xffff0000, v194
	v_lshlrev_b32_e32 v110, 16, v195
	v_and_b32_e32 v111, 0xffff0000, v195
	v_pk_fma_f32 v[110:111], v[98:99], v[136:137], v[110:111]
	v_pk_fma_f32 v[98:99], v[96:97], v[134:135], v[108:109]
	v_cvt_pk_bf16_f32 v96, v104, v105
	v_cvt_pk_bf16_f32 v97, v106, v107
	v_cvt_pk_bf16_f32 v98, v98, v99
	v_cvt_pk_bf16_f32 v99, v110, v111
	global_store_dwordx4 v[180:181], v[96:99], off offset:256
	s_nop 1
	v_lshlrev_b32_e32 v96, 16, v196
	v_and_b32_e32 v97, 0xffff0000, v196
	v_lshlrev_b32_e32 v98, 16, v197
	v_and_b32_e32 v99, 0xffff0000, v197
	v_pk_fma_f32 v[98:99], v[102:103], v[148:149], v[98:99]
	v_pk_fma_f32 v[96:97], v[100:101], v[146:147], v[96:97]
	v_lshlrev_b32_e32 v100, 16, v198
	v_and_b32_e32 v101, 0xffff0000, v198
	v_lshlrev_b32_e32 v102, 16, v199
	v_and_b32_e32 v103, 0xffff0000, v199
	v_pk_fma_f32 v[102:103], v[94:95], v[144:145], v[102:103]
	v_pk_fma_f32 v[94:95], v[92:93], v[142:143], v[100:101]
	v_cvt_pk_bf16_f32 v92, v96, v97
	v_cvt_pk_bf16_f32 v93, v98, v99
	v_cvt_pk_bf16_f32 v94, v94, v95
	v_cvt_pk_bf16_f32 v95, v102, v103
	global_store_dwordx4 v[182:183], v[92:95], off
	s_nop 1
	v_lshlrev_b32_e32 v92, 16, v200
	v_and_b32_e32 v93, 0xffff0000, v200
	v_lshlrev_b32_e32 v94, 16, v201
	v_and_b32_e32 v95, 0xffff0000, v201
	v_pk_fma_f32 v[90:91], v[90:91], v[140:141], v[94:95]
	v_pk_fma_f32 v[88:89], v[88:89], v[138:139], v[92:93]
	v_lshlrev_b32_e32 v92, 16, v202
	v_and_b32_e32 v93, 0xffff0000, v202
	v_lshlrev_b32_e32 v94, 16, v203
	v_and_b32_e32 v95, 0xffff0000, v203
	v_pk_fma_f32 v[94:95], v[82:83], v[136:137], v[94:95]
	v_pk_fma_f32 v[82:83], v[80:81], v[134:135], v[92:93]
	v_cvt_pk_bf16_f32 v80, v88, v89
	v_cvt_pk_bf16_f32 v81, v90, v91
	v_cvt_pk_bf16_f32 v82, v82, v83
	v_cvt_pk_bf16_f32 v83, v94, v95
	global_store_dwordx4 v[182:183], v[80:83], off offset:256
	s_nop 1
	v_lshlrev_b32_e32 v80, 16, v204
	v_and_b32_e32 v81, 0xffff0000, v204
	v_lshlrev_b32_e32 v82, 16, v205
	v_and_b32_e32 v83, 0xffff0000, v205
	v_pk_fma_f32 v[82:83], v[86:87], v[148:149], v[82:83]
	v_pk_fma_f32 v[80:81], v[84:85], v[146:147], v[80:81]
	v_lshlrev_b32_e32 v84, 16, v206
	v_and_b32_e32 v85, 0xffff0000, v206
	v_lshlrev_b32_e32 v86, 16, v207
	v_and_b32_e32 v87, 0xffff0000, v207
	v_pk_fma_f32 v[86:87], v[78:79], v[144:145], v[86:87]
	v_pk_fma_f32 v[78:79], v[76:77], v[142:143], v[84:85]
	v_cvt_pk_bf16_f32 v76, v80, v81
	v_cvt_pk_bf16_f32 v77, v82, v83
	v_cvt_pk_bf16_f32 v78, v78, v79
	v_cvt_pk_bf16_f32 v79, v86, v87
	global_store_dwordx4 v[170:171], v[76:79], off
	s_nop 1
	v_lshlrev_b32_e32 v76, 16, v150
	v_and_b32_e32 v77, 0xffff0000, v150
	v_lshlrev_b32_e32 v78, 16, v151
	v_and_b32_e32 v79, 0xffff0000, v151
	v_pk_fma_f32 v[74:75], v[74:75], v[140:141], v[78:79]
	v_pk_fma_f32 v[72:73], v[72:73], v[138:139], v[76:77]
	v_lshlrev_b32_e32 v76, 16, v152
	v_and_b32_e32 v77, 0xffff0000, v152
	v_lshlrev_b32_e32 v78, 16, v153
	v_and_b32_e32 v79, 0xffff0000, v153
	v_pk_fma_f32 v[78:79], v[70:71], v[136:137], v[78:79]
	v_pk_fma_f32 v[70:71], v[68:69], v[134:135], v[76:77]
	v_cvt_pk_bf16_f32 v68, v72, v73
	v_cvt_pk_bf16_f32 v69, v74, v75
	v_cvt_pk_bf16_f32 v70, v70, v71
	v_cvt_pk_bf16_f32 v71, v78, v79
	global_store_dwordx4 v[170:171], v[68:71], off offset:256
	v_add_co_u32_e32 v102, vcc, s16, v168
	s_mov_b32 s0, 0x48000
	s_nop 0
	v_addc_co_u32_e32 v103, vcc, 0, v169, vcc
	v_add_co_u32_e32 v104, vcc, s0, v168
	s_mov_b32 s0, 0x50000
	s_nop 0
	v_addc_co_u32_e32 v105, vcc, 0, v169, vcc
	v_add_co_u32_e32 v106, vcc, s0, v168
	s_mov_b32 s0, 0x58000
	s_nop 0
	v_addc_co_u32_e32 v107, vcc, 0, v169, vcc
	v_add_co_u32_e32 v68, vcc, s0, v168
	global_load_dwordx4 v[70:73], v[102:103], off
	global_load_dwordx4 v[74:77], v[102:103], off offset:256
	v_addc_co_u32_e32 v69, vcc, 0, v169, vcc
	global_load_dwordx4 v[78:81], v[104:105], off
	global_load_dwordx4 v[82:85], v[104:105], off offset:256
	global_load_dwordx4 v[86:89], v[106:107], off
	global_load_dwordx4 v[90:93], v[106:107], off offset:256
	global_load_dwordx4 v[94:97], v[68:69], off
	global_load_dwordx4 v[98:101], v[68:69], off offset:256
	s_waitcnt vmcnt(0)
	v_lshlrev_b32_e32 v108, 16, v70
	v_and_b32_e32 v109, 0xffff0000, v70
	v_lshlrev_b32_e32 v70, 16, v71
	v_and_b32_e32 v71, 0xffff0000, v71
	v_pk_fma_f32 v[66:67], v[66:67], v[148:149], v[70:71]
	v_lshlrev_b32_e32 v70, 16, v72
	v_and_b32_e32 v71, 0xffff0000, v72
	v_lshlrev_b32_e32 v72, 16, v73
	v_and_b32_e32 v73, 0xffff0000, v73
	v_pk_fma_f32 v[64:65], v[64:65], v[146:147], v[108:109]
	v_pk_fma_f32 v[72:73], v[62:63], v[144:145], v[72:73]
	v_pk_fma_f32 v[62:63], v[60:61], v[142:143], v[70:71]
	v_cvt_pk_bf16_f32 v60, v64, v65
	v_cvt_pk_bf16_f32 v61, v66, v67
	v_cvt_pk_bf16_f32 v62, v62, v63
	v_cvt_pk_bf16_f32 v63, v72, v73
	global_store_dwordx4 v[102:103], v[60:63], off
	s_nop 1
	v_lshlrev_b32_e32 v60, 16, v74
	v_and_b32_e32 v61, 0xffff0000, v74
	v_lshlrev_b32_e32 v62, 16, v75
	v_and_b32_e32 v63, 0xffff0000, v75
	v_pk_fma_f32 v[58:59], v[58:59], v[140:141], v[62:63]
	v_pk_fma_f32 v[56:57], v[56:57], v[138:139], v[60:61]
	v_lshlrev_b32_e32 v60, 16, v76
	v_and_b32_e32 v61, 0xffff0000, v76
	v_lshlrev_b32_e32 v62, 16, v77
	v_and_b32_e32 v63, 0xffff0000, v77
	v_pk_fma_f32 v[62:63], v[50:51], v[136:137], v[62:63]
	v_pk_fma_f32 v[50:51], v[48:49], v[134:135], v[60:61]
	v_cvt_pk_bf16_f32 v48, v56, v57
	v_cvt_pk_bf16_f32 v49, v58, v59
	v_cvt_pk_bf16_f32 v50, v50, v51
	v_cvt_pk_bf16_f32 v51, v62, v63
	global_store_dwordx4 v[102:103], v[48:51], off offset:256
	s_nop 1
	v_lshlrev_b32_e32 v48, 16, v78
	v_and_b32_e32 v49, 0xffff0000, v78
	v_lshlrev_b32_e32 v50, 16, v79
	v_and_b32_e32 v51, 0xffff0000, v79
	v_pk_fma_f32 v[50:51], v[54:55], v[148:149], v[50:51]
	v_pk_fma_f32 v[48:49], v[52:53], v[146:147], v[48:49]
	v_lshlrev_b32_e32 v52, 16, v80
	v_and_b32_e32 v53, 0xffff0000, v80
	v_lshlrev_b32_e32 v54, 16, v81
	v_and_b32_e32 v55, 0xffff0000, v81
	v_pk_fma_f32 v[54:55], v[46:47], v[144:145], v[54:55]
	v_pk_fma_f32 v[46:47], v[44:45], v[142:143], v[52:53]
	v_cvt_pk_bf16_f32 v44, v48, v49
	v_cvt_pk_bf16_f32 v45, v50, v51
	v_cvt_pk_bf16_f32 v46, v46, v47
	v_cvt_pk_bf16_f32 v47, v54, v55
	global_store_dwordx4 v[104:105], v[44:47], off
	s_nop 1
	v_lshlrev_b32_e32 v44, 16, v82
	v_and_b32_e32 v45, 0xffff0000, v82
	v_lshlrev_b32_e32 v46, 16, v83
	v_and_b32_e32 v47, 0xffff0000, v83
	v_pk_fma_f32 v[34:35], v[34:35], v[140:141], v[46:47]
	v_pk_fma_f32 v[32:33], v[32:33], v[138:139], v[44:45]
	v_lshlrev_b32_e32 v44, 16, v84
	v_and_b32_e32 v45, 0xffff0000, v84
	v_lshlrev_b32_e32 v46, 16, v85
	v_and_b32_e32 v47, 0xffff0000, v85
	v_pk_fma_f32 v[46:47], v[22:23], v[136:137], v[46:47]
	v_pk_fma_f32 v[22:23], v[20:21], v[134:135], v[44:45]
	v_cvt_pk_bf16_f32 v20, v32, v33
	v_cvt_pk_bf16_f32 v21, v34, v35
	v_cvt_pk_bf16_f32 v22, v22, v23
	v_cvt_pk_bf16_f32 v23, v46, v47
	global_store_dwordx4 v[104:105], v[20:23], off offset:256
	s_nop 1
	v_lshlrev_b32_e32 v20, 16, v86
	v_and_b32_e32 v21, 0xffff0000, v86
	v_lshlrev_b32_e32 v22, 16, v87
	v_and_b32_e32 v23, 0xffff0000, v87
	v_pk_fma_f32 v[22:23], v[30:31], v[148:149], v[22:23]
	v_pk_fma_f32 v[20:21], v[28:29], v[146:147], v[20:21]
	v_lshlrev_b32_e32 v28, 16, v88
	v_and_b32_e32 v29, 0xffff0000, v88
	v_lshlrev_b32_e32 v30, 16, v89
	v_and_b32_e32 v31, 0xffff0000, v89
	v_pk_fma_f32 v[30:31], v[14:15], v[144:145], v[30:31]
	v_pk_fma_f32 v[14:15], v[12:13], v[142:143], v[28:29]
	v_cvt_pk_bf16_f32 v12, v20, v21
	v_cvt_pk_bf16_f32 v13, v22, v23
	v_cvt_pk_bf16_f32 v14, v14, v15
	v_cvt_pk_bf16_f32 v15, v30, v31
	global_store_dwordx4 v[106:107], v[12:15], off
	v_lshlrev_b32_e32 v20, 16, v92
	v_and_b32_e32 v21, 0xffff0000, v92
	v_lshlrev_b32_e32 v12, 16, v90
	v_and_b32_e32 v13, 0xffff0000, v90
	v_lshlrev_b32_e32 v14, 16, v91
	v_and_b32_e32 v15, 0xffff0000, v91
	v_lshlrev_b32_e32 v22, 16, v93
	v_and_b32_e32 v23, 0xffff0000, v93
	v_pk_fma_f32 v[14:15], v[42:43], v[140:141], v[14:15]
	v_pk_fma_f32 v[12:13], v[40:41], v[138:139], v[12:13]
	v_pk_fma_f32 v[22:23], v[38:39], v[136:137], v[22:23]
	v_pk_fma_f32 v[20:21], v[36:37], v[134:135], v[20:21]
	v_cvt_pk_bf16_f32 v12, v12, v13
	v_cvt_pk_bf16_f32 v13, v14, v15
	v_cvt_pk_bf16_f32 v14, v20, v21
	v_cvt_pk_bf16_f32 v15, v22, v23
	global_store_dwordx4 v[106:107], v[12:15], off offset:256
	s_nop 1
	v_lshlrev_b32_e32 v12, 16, v94
	v_and_b32_e32 v13, 0xffff0000, v94
	v_lshlrev_b32_e32 v14, 16, v95
	v_and_b32_e32 v15, 0xffff0000, v95
	v_pk_fma_f32 v[10:11], v[10:11], v[148:149], v[14:15]
	v_pk_fma_f32 v[8:9], v[8:9], v[146:147], v[12:13]
	v_lshlrev_b32_e32 v12, 16, v96
	v_and_b32_e32 v13, 0xffff0000, v96
	v_lshlrev_b32_e32 v14, 16, v97
	v_and_b32_e32 v15, 0xffff0000, v97
	v_pk_fma_f32 v[14:15], v[6:7], v[144:145], v[14:15]
	v_pk_fma_f32 v[6:7], v[4:5], v[142:143], v[12:13]
	v_cvt_pk_bf16_f32 v4, v8, v9
	v_cvt_pk_bf16_f32 v5, v10, v11
	v_cvt_pk_bf16_f32 v6, v6, v7
	v_cvt_pk_bf16_f32 v7, v14, v15
	global_store_dwordx4 v[68:69], v[4:7], off
	v_lshlrev_b32_e32 v8, 16, v100
	v_and_b32_e32 v9, 0xffff0000, v100
	v_lshlrev_b32_e32 v4, 16, v98
	v_and_b32_e32 v5, 0xffff0000, v98
	v_lshlrev_b32_e32 v6, 16, v99
	v_and_b32_e32 v7, 0xffff0000, v99
	v_lshlrev_b32_e32 v10, 16, v101
	v_and_b32_e32 v11, 0xffff0000, v101
	v_pk_fma_f32 v[6:7], v[26:27], v[140:141], v[6:7]
	v_pk_fma_f32 v[4:5], v[24:25], v[138:139], v[4:5]
	v_pk_fma_f32 v[10:11], v[18:19], v[136:137], v[10:11]
	v_pk_fma_f32 v[8:9], v[16:17], v[134:135], v[8:9]
	v_cvt_pk_bf16_f32 v4, v4, v5
	v_cvt_pk_bf16_f32 v5, v6, v7
	v_cvt_pk_bf16_f32 v6, v8, v9
	v_cvt_pk_bf16_f32 v7, v10, v11
	global_store_dwordx4 v[68:69], v[4:7], off offset:256
	s_and_b64 vcc, exec, s[38:39]
	s_mov_b32 s69, s67
	s_mov_b32 s70, s68
	s_mov_b64 s[50:51], s[48:49]
	s_mov_b64 s[52:53], s[46:47]
	s_cbranch_vccz .LBB0_803
	s_waitcnt vmcnt(0)
	s_cmpk_gt_u32 s6, 0xff
	s_cbranch_scc1 .LBB0_810
	s_barrier

.LBB0_961:
	s_add_u32 s0, s40, 0x100
	s_addc_u32 s1, s41, 0
	s_mov_b32 s76, -2
.Lpeelqa_hdr:
	s_add_u32 s40, s42, 0x100
	s_addc_u32 s41, s43, 0
	s_cmp_eq_u32 s76, 4
	s_cselect_b32 s59, s55, s41
	s_cselect_b32 s58, s54, s40
	s_cselect_b32 s45, s57, s1
	s_cselect_b32 s44, s56, s0
	s_add_i32 s78, 0, 0x10400
	v_add_u32_e32 v2, s78, v214
	ds_read_b128 v[12:15], v2
	ds_read_b128 v[16:19], v2 offset:1024
	ds_read_b128 v[4:7], v2 offset:2048
	ds_read_b128 v[8:11], v2 offset:3072
	v_lshl_add_u64 v[20:21], s[42:43], 0, v[204:205]
	s_add_i32 m0, s64, 0xc400
	ds_read_b128 v[170:173], v216 offset:1024
	ds_read_b128 v[174:177], v216 offset:2048
	ds_read_b128 v[218:221], v216 offset:3072
	ds_read_b128 v[222:225], v216 offset:4096
	ds_read_b128 v[240:243], v216 offset:5120
	ds_read_b128 v[244:247], v216 offset:6144
	ds_read_b128 v[230:233], v216 offset:7168
	ds_read_b128 v[234:237], v216 offset:8192
	global_load_lds_dwordx4 v[20:21], off
	v_lshl_add_u64 v[20:21], s[42:43], 0, v[202:203]
	s_add_i32 m0, s64, 0xe400
	s_nop 0
	global_load_lds_dwordx4 v[20:21], off
	s_waitcnt lgkmcnt(8)
	s_barrier
	s_waitcnt lgkmcnt(0)
	s_setprio 1
	s_waitcnt lgkmcnt(0)
	v_mfma_scale_f32_16x16x128_f8f6f4 v[162:165], v[12:19], v[170:177], 0, v117, v212 op_sel_hi:[0,0,0]
	v_mfma_scale_f32_16x16x128_f8f6f4 v[154:157], v[4:11], v[170:177], 0, v117, v212 op_sel_hi:[0,0,0]
	v_mfma_scale_f32_16x16x128_f8f6f4 v[146:149], v[12:19], v[218:225], 0, v117, v212 op_sel_hi:[0,0,0]
	v_mfma_scale_f32_16x16x128_f8f6f4 v[138:141], v[4:11], v[218:225], 0, v117, v212 op_sel_hi:[0,0,0]
	v_mfma_scale_f32_16x16x128_f8f6f4 v[130:133], v[12:19], v[240:247], 0, v117, v212 op_sel_hi:[0,0,0]
	v_mfma_scale_f32_16x16x128_f8f6f4 v[122:125], v[4:11], v[240:247], 0, v117, v212 op_sel_hi:[0,0,0]
	v_mfma_scale_f32_16x16x128_f8f6f4 v[112:115], v[12:19], v[230:237], 0, v117, v212 op_sel_hi:[0,0,0]
	v_mfma_scale_f32_16x16x128_f8f6f4 v[104:107], v[4:11], v[230:237], 0, v117, v212 op_sel_hi:[0,0,0]
	s_setprio 0
	s_barrier
	s_add_i32 s42, 0, 0x14400
	s_add_i32 s43, s78, s61
	v_add_u32_e32 v2, s42, v214
	v_lshl_add_u64 v[166:167], s[44:45], 0, v[184:185]
	s_mov_b32 m0, s43
	ds_read_b128 v[28:31], v2
	ds_read_b128 v[32:35], v2 offset:1024
	ds_read_b128 v[20:23], v2 offset:2048
	ds_read_b128 v[24:27], v2 offset:3072
	global_load_lds_dwordx4 v[166:167], off
	v_lshl_add_u64 v[168:169], s[44:45], 0, v[186:187]
	s_add_i32 m0, s43, 0x2000
	s_nop 0
	global_load_lds_dwordx4 v[168:169], off
	s_barrier
	s_waitcnt lgkmcnt(0)
	s_setprio 1
	s_waitcnt lgkmcnt(0)
	v_mfma_scale_f32_16x16x128_f8f6f4 v[158:161], v[28:35], v[170:177], 0, v117, v212 op_sel_hi:[0,0,0]
	v_mfma_scale_f32_16x16x128_f8f6f4 v[150:153], v[20:27], v[170:177], 0, v117, v212 op_sel_hi:[0,0,0]
	v_mfma_scale_f32_16x16x128_f8f6f4 v[142:145], v[28:35], v[218:225], 0, v117, v212 op_sel_hi:[0,0,0]
	v_mfma_scale_f32_16x16x128_f8f6f4 v[134:137], v[20:27], v[218:225], 0, v117, v212 op_sel_hi:[0,0,0]
	v_mfma_scale_f32_16x16x128_f8f6f4 v[126:129], v[28:35], v[240:247], 0, v117, v212 op_sel_hi:[0,0,0]
	v_mfma_scale_f32_16x16x128_f8f6f4 v[118:121], v[20:27], v[240:247], 0, v117, v212 op_sel_hi:[0,0,0]
	v_mfma_scale_f32_16x16x128_f8f6f4 v[108:111], v[28:35], v[230:237], 0, v117, v212 op_sel_hi:[0,0,0]
	v_mfma_scale_f32_16x16x128_f8f6f4 v[100:103], v[20:27], v[230:237], 0, v117, v212 op_sel_hi:[0,0,0]
	s_setprio 0
	s_mov_b32 m0, s65
	v_lshl_add_u64 v[170:171], s[58:59], 0, v[188:189]
	s_barrier
	ds_read_b128 v[174:177], v216 offset:17408
	ds_read_b128 v[178:181], v216 offset:18432
	ds_read_b128 v[218:221], v216 offset:19456
	ds_read_b128 v[222:225], v216 offset:20480
	ds_read_b128 v[230:233], v216 offset:21504
	ds_read_b128 v[234:237], v216 offset:22528
	ds_read_b128 v[240:243], v216 offset:23552
	ds_read_b128 v[244:247], v216 offset:24576
	global_load_lds_dwordx4 v[170:171], off
	v_lshl_add_u64 v[172:173], s[58:59], 0, v[190:191]
	s_mov_b32 m0, s66
	s_nop 0
	global_load_lds_dwordx4 v[172:173], off
	s_barrier
	s_waitcnt lgkmcnt(0)
	s_setprio 1
	s_waitcnt lgkmcnt(0)
	v_mfma_scale_f32_16x16x128_f8f6f4 v[96:99], v[12:19], v[174:181], 0, v117, v212 op_sel_hi:[0,0,0]
	v_mfma_scale_f32_16x16x128_f8f6f4 v[88:91], v[4:11], v[174:181], 0, v117, v212 op_sel_hi:[0,0,0]
	v_mfma_scale_f32_16x16x128_f8f6f4 v[80:83], v[12:19], v[218:225], 0, v117, v212 op_sel_hi:[0,0,0]
	v_mfma_scale_f32_16x16x128_f8f6f4 v[72:75], v[4:11], v[218:225], 0, v117, v212 op_sel_hi:[0,0,0]
	v_mfma_scale_f32_16x16x128_f8f6f4 v[60:63], v[12:19], v[230:237], 0, v117, v212 op_sel_hi:[0,0,0]
	v_mfma_scale_f32_16x16x128_f8f6f4 v[48:51], v[4:11], v[230:237], 0, v117, v212 op_sel_hi:[0,0,0]
	v_mfma_scale_f32_16x16x128_f8f6f4 v[40:43], v[12:19], v[240:247], 0, v117, v212 op_sel_hi:[0,0,0]
	v_mfma_scale_f32_16x16x128_f8f6f4 v[36:39], v[4:11], v[240:247], 0, v117, v212 op_sel_hi:[0,0,0]
	s_setprio 0
	s_barrier
	s_add_u32 s78, s44, 0x20000
	s_addc_u32 s79, s45, 0
	s_add_i32 s42, s42, s61
	v_lshl_add_u64 v[4:5], s[78:79], 0, v[184:185]
	s_mov_b32 m0, s42
	s_nop 0
	global_load_lds_dwordx4 v[4:5], off
	v_lshl_add_u64 v[4:5], s[78:79], 0, v[186:187]
	s_add_i32 m0, s42, 0x2000
	s_nop 0
	global_load_lds_dwordx4 v[4:5], off
	s_waitcnt vmcnt(6)
	s_barrier
	s_setprio 1
	v_mfma_scale_f32_16x16x128_f8f6f4 v[92:95], v[28:35], v[174:181], 0, v117, v212 op_sel_hi:[0,0,0]
	v_mfma_scale_f32_16x16x128_f8f6f4 v[84:87], v[20:27], v[174:181], 0, v117, v212 op_sel_hi:[0,0,0]
	v_mfma_scale_f32_16x16x128_f8f6f4 v[76:79], v[28:35], v[218:225], 0, v117, v212 op_sel_hi:[0,0,0]
	v_mfma_scale_f32_16x16x128_f8f6f4 v[64:67], v[20:27], v[218:225], 0, v117, v212 op_sel_hi:[0,0,0]
	v_mfma_scale_f32_16x16x128_f8f6f4 v[68:71], v[28:35], v[230:237], 0, v117, v212 op_sel_hi:[0,0,0]
	v_mfma_scale_f32_16x16x128_f8f6f4 v[56:59], v[20:27], v[230:237], 0, v117, v212 op_sel_hi:[0,0,0]
	v_mfma_scale_f32_16x16x128_f8f6f4 v[52:55], v[28:35], v[240:247], 0, v117, v212 op_sel_hi:[0,0,0]
	v_mfma_scale_f32_16x16x128_f8f6f4 v[44:47], v[20:27], v[240:247], 0, v117, v212 op_sel_hi:[0,0,0]
	s_setprio 0
	s_add_i32 s42, 0, 0x18400
	v_add_u32_e32 v2, s42, v214
	s_barrier
	ds_read_b128 v[12:15], v2
	ds_read_b128 v[16:19], v2 offset:1024
	ds_read_b128 v[4:7], v2 offset:2048
	ds_read_b128 v[8:11], v2 offset:3072
	s_mov_b32 m0, s67
	v_lshl_add_u64 v[182:183], s[58:59], 0, v[192:193]
	ds_read_b128 v[20:23], v216 offset:33792
	ds_read_b128 v[24:27], v216 offset:34816
	ds_read_b128 v[28:31], v216 offset:35840
	ds_read_b128 v[32:35], v216 offset:36864
	ds_read_b128 v[174:177], v216 offset:37888
	ds_read_b128 v[178:181], v216 offset:38912
	ds_read_b128 v[218:221], v216 offset:39936
	ds_read_b128 v[222:225], v216 offset:40960
	global_load_lds_dwordx4 v[182:183], off
	v_lshl_add_u64 v[182:183], s[58:59], 0, v[194:195]
	s_mov_b32 m0, s68
	s_nop 0
	global_load_lds_dwordx4 v[182:183], off
	s_waitcnt lgkmcnt(8)
	s_barrier
	s_waitcnt lgkmcnt(0)
	s_setprio 1
	s_waitcnt lgkmcnt(0)
	v_mfma_scale_f32_16x16x128_f8f6f4 v[162:165], v[12:19], v[20:27], v[162:165], v117, v212 op_sel_hi:[0,0,0]
	v_mfma_scale_f32_16x16x128_f8f6f4 v[154:157], v[4:11], v[20:27], v[154:157], v117, v212 op_sel_hi:[0,0,0]
	v_mfma_scale_f32_16x16x128_f8f6f4 v[146:149], v[12:19], v[28:35], v[146:149], v117, v212 op_sel_hi:[0,0,0]
	v_mfma_scale_f32_16x16x128_f8f6f4 v[138:141], v[4:11], v[28:35], v[138:141], v117, v212 op_sel_hi:[0,0,0]
	v_mfma_scale_f32_16x16x128_f8f6f4 v[130:133], v[12:19], v[174:181], v[130:133], v117, v212 op_sel_hi:[0,0,0]
	v_mfma_scale_f32_16x16x128_f8f6f4 v[122:125], v[4:11], v[174:181], v[122:125], v117, v212 op_sel_hi:[0,0,0]
	v_mfma_scale_f32_16x16x128_f8f6f4 v[112:115], v[12:19], v[218:225], v[112:115], v117, v212 op_sel_hi:[0,0,0]
	v_mfma_scale_f32_16x16x128_f8f6f4 v[104:107], v[4:11], v[218:225], v[104:107], v117, v212 op_sel_hi:[0,0,0]
	s_setprio 0
	s_barrier
	s_add_i32 s58, 0, 0x1c400
	s_add_i32 s42, s42, s61
	v_add_u32_e32 v2, s58, v214
	v_lshl_add_u64 v[166:167], v[166:167], 0, s[22:23]
	s_mov_b32 m0, s42
	ds_read_b128 v[230:233], v2
	ds_read_b128 v[234:237], v2 offset:1024
	ds_read_b128 v[240:243], v2 offset:2048
	ds_read_b128 v[244:247], v2 offset:3072
	global_load_lds_dwordx4 v[166:167], off
	v_lshl_add_u64 v[166:167], v[168:169], 0, s[22:23]
	s_add_i32 m0, s42, 0x2000
	s_nop 0
	global_load_lds_dwordx4 v[166:167], off
	s_barrier
	s_waitcnt lgkmcnt(0)
	s_setprio 1
	s_waitcnt lgkmcnt(0)
	v_mfma_scale_f32_16x16x128_f8f6f4 v[158:161], v[230:237], v[20:27], v[158:161], v117, v212 op_sel_hi:[0,0,0]
	v_mfma_scale_f32_16x16x128_f8f6f4 v[150:153], v[240:247], v[20:27], v[150:153], v117, v212 op_sel_hi:[0,0,0]
	v_mfma_scale_f32_16x16x128_f8f6f4 v[142:145], v[230:237], v[28:35], v[142:145], v117, v212 op_sel_hi:[0,0,0]
	v_mfma_scale_f32_16x16x128_f8f6f4 v[134:137], v[240:247], v[28:35], v[134:137], v117, v212 op_sel_hi:[0,0,0]
	v_mfma_scale_f32_16x16x128_f8f6f4 v[126:129], v[230:237], v[174:181], v[126:129], v117, v212 op_sel_hi:[0,0,0]
	v_mfma_scale_f32_16x16x128_f8f6f4 v[118:121], v[240:247], v[174:181], v[118:121], v117, v212 op_sel_hi:[0,0,0]
	v_mfma_scale_f32_16x16x128_f8f6f4 v[108:111], v[230:237], v[218:225], v[108:111], v117, v212 op_sel_hi:[0,0,0]
	v_mfma_scale_f32_16x16x128_f8f6f4 v[100:103], v[240:247], v[218:225], v[100:103], v117, v212 op_sel_hi:[0,0,0]
	s_setprio 0
	s_mov_b32 m0, s71
	v_lshl_add_u64 v[166:167], v[170:171], 0, s[22:23]
	s_barrier
	ds_read_b128 v[20:23], v216 offset:50176
	ds_read_b128 v[24:27], v216 offset:51200
	ds_read_b128 v[28:31], v216 offset:52224
	ds_read_b128 v[32:35], v216 offset:53248
	ds_read_b128 v[174:177], v216 offset:54272
	ds_read_b128 v[178:181], v216 offset:55296
	ds_read_b128 v[218:221], v216 offset:56320
	ds_read_b128 v[222:225], v216 offset:57344
	global_load_lds_dwordx4 v[166:167], off
	v_lshl_add_u64 v[166:167], v[172:173], 0, s[22:23]
	s_mov_b32 m0, s72
	s_nop 0
	global_load_lds_dwordx4 v[166:167], off
	s_barrier
	s_waitcnt lgkmcnt(0)
	s_setprio 1
	s_waitcnt lgkmcnt(0)
	v_mfma_scale_f32_16x16x128_f8f6f4 v[96:99], v[12:19], v[20:27], v[96:99], v117, v212 op_sel_hi:[0,0,0]
	v_mfma_scale_f32_16x16x128_f8f6f4 v[88:91], v[4:11], v[20:27], v[88:91], v117, v212 op_sel_hi:[0,0,0]
	v_mfma_scale_f32_16x16x128_f8f6f4 v[80:83], v[12:19], v[28:35], v[80:83], v117, v212 op_sel_hi:[0,0,0]
	v_mfma_scale_f32_16x16x128_f8f6f4 v[72:75], v[4:11], v[28:35], v[72:75], v117, v212 op_sel_hi:[0,0,0]
	v_mfma_scale_f32_16x16x128_f8f6f4 v[60:63], v[12:19], v[174:181], v[60:63], v117, v212 op_sel_hi:[0,0,0]
	v_mfma_scale_f32_16x16x128_f8f6f4 v[48:51], v[4:11], v[174:181], v[48:51], v117, v212 op_sel_hi:[0,0,0]
	v_mfma_scale_f32_16x16x128_f8f6f4 v[40:43], v[12:19], v[218:225], v[40:43], v117, v212 op_sel_hi:[0,0,0]
	v_mfma_scale_f32_16x16x128_f8f6f4 v[36:39], v[4:11], v[218:225], v[36:39], v117, v212 op_sel_hi:[0,0,0]
	s_setprio 0
	s_barrier
	s_add_u32 s42, s44, 0x20080
	s_addc_u32 s43, s45, 0
	s_add_i32 s44, s58, s61
	v_lshl_add_u64 v[4:5], s[42:43], 0, v[184:185]
	s_mov_b32 m0, s44
	s_nop 0
	global_load_lds_dwordx4 v[4:5], off
	v_lshl_add_u64 v[4:5], s[42:43], 0, v[186:187]
	s_add_i32 m0, s44, 0x2000
	s_nop 0
	global_load_lds_dwordx4 v[4:5], off
	s_waitcnt vmcnt(6)
	s_barrier
	s_setprio 1
	v_mfma_scale_f32_16x16x128_f8f6f4 v[92:95], v[230:237], v[20:27], v[92:95], v117, v212 op_sel_hi:[0,0,0]
	v_mfma_scale_f32_16x16x128_f8f6f4 v[84:87], v[240:247], v[20:27], v[84:87], v117, v212 op_sel_hi:[0,0,0]
	v_mfma_scale_f32_16x16x128_f8f6f4 v[76:79], v[230:237], v[28:35], v[76:79], v117, v212 op_sel_hi:[0,0,0]
	v_mfma_scale_f32_16x16x128_f8f6f4 v[64:67], v[240:247], v[28:35], v[64:67], v117, v212 op_sel_hi:[0,0,0]
	v_mfma_scale_f32_16x16x128_f8f6f4 v[68:71], v[230:237], v[174:181], v[68:71], v117, v212 op_sel_hi:[0,0,0]
	v_mfma_scale_f32_16x16x128_f8f6f4 v[56:59], v[240:247], v[174:181], v[56:59], v117, v212 op_sel_hi:[0,0,0]
	v_mfma_scale_f32_16x16x128_f8f6f4 v[52:55], v[230:237], v[218:225], v[52:55], v117, v212 op_sel_hi:[0,0,0]
	v_mfma_scale_f32_16x16x128_f8f6f4 v[44:47], v[240:247], v[218:225], v[44:47], v117, v212 op_sel_hi:[0,0,0]
	s_setprio 0
	s_add_i32 s76, s76, 2
	s_add_u32 s0, s0, 0x100
	s_addc_u32 s1, s1, 0
	s_cmp_gt_u32 s76, 5
	s_mov_b64 s[42:43], s[40:41]
	s_barrier
	s_cbranch_scc0 .LBB0_962
	s_branch .Lpexit_qa

.Lpexit_qa:
	s_cmp_eq_u32 s3, 5
	s_cselect_b64 s[0:1], -1, 0
	s_cmpk_gt_i32 s6, 0x7f
	s_nop 15
	s_nop 15
	s_cselect_b64 s[40:41], -1, 0
	s_or_b64 s[40:41], s[40:41], s[0:1]
	s_lshl_b32 s6, s6, 8
	s_and_b64 vcc, exec, s[40:41]
	s_cbranch_vccnz .LBB0_965
	s_lshr_b32 s0, s6, 6
	s_add_i32 s0, s0, s25
	s_lshl_b32 s0, s0, 4
	s_and_b32 s1, s0, 0x3f0
	v_or_b32_e32 v2, s1, v215
	s_add_i32 s0, s0, 32
	v_lshlrev_b32_e32 v2, 3, v2
	s_and_b32 s0, s0, 0x3f0
	global_load_dwordx4 v[4:7], v[200:201], off offset:16
	global_load_dwordx4 v[8:11], v[200:201], off
	global_load_dwordx4 v[20:23], v[198:199], off offset:16
	global_load_dwordx4 v[24:27], v[198:199], off
	global_load_dwordx4 v[28:31], v[196:197], off offset:2064
	global_load_dwordx4 v[32:35], v[196:197], off offset:2048
	global_load_dwordx4 v[166:169], v[196:197], off offset:16
	global_load_dwordx4 v[170:173], v[196:197], off
	global_load_dwordx4 v[174:177], v2, s[46:47] offset:16
	global_load_dwordx4 v[178:181], v2, s[46:47]
	v_or_b32_e32 v2, s0, v215
	v_lshlrev_b32_e32 v2, 3, v2
	global_load_dwordx4 v[12:15], v2, s[46:47] offset:16
	global_load_dwordx4 v[16:19], v2, s[46:47]
	s_waitcnt vmcnt(0)
	v_mov_b32_e32 v206, v5
	v_mov_b32_e32 v5, v6
	v_mov_b32_e32 v207, v7
	v_mov_b32_e32 v6, v9
	v_mov_b32_e32 v9, v10
	v_mov_b32_e32 v7, v11
	v_mov_b32_e32 v208, v21
	v_mov_b32_e32 v21, v22
	v_mov_b32_e32 v209, v23
	v_mov_b32_e32 v22, v25
	v_mov_b32_e32 v25, v26
	v_mov_b32_e32 v23, v27
	v_mov_b32_e32 v26, v29
	v_mov_b32_e32 v29, v30
	v_mov_b32_e32 v27, v31
	v_mov_b32_e32 v30, v33
	v_mov_b32_e32 v33, v34
	v_mov_b32_e32 v31, v35
	v_mov_b32_e32 v34, v167
	v_mov_b32_e32 v167, v168
	v_mov_b32_e32 v35, v169
	v_mov_b32_e32 v168, v171
	v_mov_b32_e32 v171, v172
	v_mov_b32_e32 v210, v175
	v_mov_b32_e32 v175, v176
	v_mov_b32_e32 v211, v177
	v_mov_b32_e32 v176, v179
	v_mov_b32_e32 v179, v180
	v_mov_b32_e32 v177, v181
	v_mov_b32_e32 v10, v13
	v_mov_b32_e32 v13, v14
	v_mov_b32_e32 v11, v15
	v_mov_b32_e32 v14, v17
	v_mov_b32_e32 v17, v18
	v_mov_b32_e32 v15, v19
	v_mov_b32_e32 v169, v173

.LBB0_1043:
	s_add_u32 s0, s44, 0x100
	s_addc_u32 s1, s45, 0
	s_mov_b32 s3, -2
.Lpeelqb_hdr:
	s_add_u32 s44, s46, 0x100
	s_addc_u32 s45, s47, 0
	s_cmp_eq_u32 s3, 4
	s_cselect_b32 s61, s55, s45
	s_cselect_b32 s60, s54, s44
	s_cselect_b32 s59, s57, s1
	s_cselect_b32 s58, s56, s0
	s_add_i32 s87, 0, 0x10400
	v_add_u32_e32 v2, s87, v241
	ds_read_b128 v[12:15], v2
	ds_read_b128 v[16:19], v2 offset:1024
	ds_read_b128 v[4:7], v2 offset:2048
	ds_read_b128 v[8:11], v2 offset:3072
	v_lshl_add_u64 v[20:21], s[46:47], 0, v[200:201]
	s_add_i32 m0, s65, 0xc400
	ds_read_b128 v[170:173], v248 offset:1024
	ds_read_b128 v[174:177], v248 offset:2048
	ds_read_b128 v[202:205], v248 offset:3072
	ds_read_b128 v[206:209], v248 offset:4096
	ds_read_b128 v[210:213], v248 offset:5120
	ds_read_b128 v[214:217], v248 offset:6144
	ds_read_b128 v[218:221], v248 offset:7168
	ds_read_b128 v[222:225], v248 offset:8192
	global_load_lds_dwordx4 v[20:21], off
	v_lshl_add_u64 v[20:21], s[46:47], 0, v[198:199]
	s_add_i32 m0, s65, 0xe400
	s_nop 0
	global_load_lds_dwordx4 v[20:21], off
	s_waitcnt lgkmcnt(8)
	s_barrier
	s_waitcnt lgkmcnt(0)
	s_setprio 1
	s_waitcnt lgkmcnt(0)
	v_mfma_scale_f32_16x16x128_f8f6f4 v[162:165], v[12:19], v[170:177], 0, v117, v197 op_sel_hi:[0,0,0]
	v_mfma_scale_f32_16x16x128_f8f6f4 v[154:157], v[4:11], v[170:177], 0, v117, v197 op_sel_hi:[0,0,0]
	v_mfma_scale_f32_16x16x128_f8f6f4 v[146:149], v[12:19], v[202:209], 0, v117, v197 op_sel_hi:[0,0,0]
	v_mfma_scale_f32_16x16x128_f8f6f4 v[138:141], v[4:11], v[202:209], 0, v117, v197 op_sel_hi:[0,0,0]
	v_mfma_scale_f32_16x16x128_f8f6f4 v[96:99], v[12:19], v[210:217], 0, v117, v197 op_sel_hi:[0,0,0]
	v_mfma_scale_f32_16x16x128_f8f6f4 v[88:91], v[4:11], v[210:217], 0, v117, v197 op_sel_hi:[0,0,0]
	v_mfma_scale_f32_16x16x128_f8f6f4 v[80:83], v[12:19], v[218:225], 0, v117, v197 op_sel_hi:[0,0,0]
	v_mfma_scale_f32_16x16x128_f8f6f4 v[72:75], v[4:11], v[218:225], 0, v117, v197 op_sel_hi:[0,0,0]
	s_setprio 0
	s_barrier
	s_add_i32 s6, 0, 0x14400
	s_add_i32 s46, s87, s64
	v_add_u32_e32 v2, s6, v241
	v_lshl_add_u64 v[166:167], s[58:59], 0, v[184:185]
	s_mov_b32 m0, s46
	ds_read_b128 v[28:31], v2
	ds_read_b128 v[32:35], v2 offset:1024
	ds_read_b128 v[20:23], v2 offset:2048
	ds_read_b128 v[24:27], v2 offset:3072
	global_load_lds_dwordx4 v[166:167], off
	v_lshl_add_u64 v[168:169], s[58:59], 0, v[186:187]
	s_add_i32 m0, s46, 0x2000
	s_nop 0
	global_load_lds_dwordx4 v[168:169], off
	s_barrier
	s_waitcnt lgkmcnt(0)
	s_setprio 1
	s_waitcnt lgkmcnt(0)
	v_mfma_scale_f32_16x16x128_f8f6f4 v[158:161], v[28:35], v[170:177], 0, v117, v197 op_sel_hi:[0,0,0]
	v_mfma_scale_f32_16x16x128_f8f6f4 v[150:153], v[20:27], v[170:177], 0, v117, v197 op_sel_hi:[0,0,0]
	v_mfma_scale_f32_16x16x128_f8f6f4 v[142:145], v[28:35], v[202:209], 0, v117, v197 op_sel_hi:[0,0,0]
	v_mfma_scale_f32_16x16x128_f8f6f4 v[134:137], v[20:27], v[202:209], 0, v117, v197 op_sel_hi:[0,0,0]
	v_mfma_scale_f32_16x16x128_f8f6f4 v[92:95], v[28:35], v[210:217], 0, v117, v197 op_sel_hi:[0,0,0]
	v_mfma_scale_f32_16x16x128_f8f6f4 v[84:87], v[20:27], v[210:217], 0, v117, v197 op_sel_hi:[0,0,0]
	v_mfma_scale_f32_16x16x128_f8f6f4 v[76:79], v[28:35], v[218:225], 0, v117, v197 op_sel_hi:[0,0,0]
	v_mfma_scale_f32_16x16x128_f8f6f4 v[68:71], v[20:27], v[218:225], 0, v117, v197 op_sel_hi:[0,0,0]
	s_setprio 0
	s_mov_b32 m0, s66
	v_lshl_add_u64 v[170:171], s[60:61], 0, v[188:189]
	s_barrier
	ds_read_b128 v[174:177], v248 offset:17408
	ds_read_b128 v[178:181], v248 offset:18432
	ds_read_b128 v[202:205], v248 offset:19456
	ds_read_b128 v[206:209], v248 offset:20480
	ds_read_b128 v[210:213], v248 offset:21504
	ds_read_b128 v[214:217], v248 offset:22528
	ds_read_b128 v[218:221], v248 offset:23552
	ds_read_b128 v[222:225], v248 offset:24576
	global_load_lds_dwordx4 v[170:171], off
	v_lshl_add_u64 v[172:173], s[60:61], 0, v[190:191]
	s_mov_b32 m0, s67
	s_nop 0
	global_load_lds_dwordx4 v[172:173], off
	s_barrier
	s_waitcnt lgkmcnt(0)
	s_setprio 1
	s_waitcnt lgkmcnt(0)
	v_mfma_scale_f32_16x16x128_f8f6f4 v[130:133], v[12:19], v[174:181], 0, v117, v197 op_sel_hi:[0,0,0]
	v_mfma_scale_f32_16x16x128_f8f6f4 v[122:125], v[4:11], v[174:181], 0, v117, v197 op_sel_hi:[0,0,0]
	v_mfma_scale_f32_16x16x128_f8f6f4 v[112:115], v[12:19], v[202:209], 0, v117, v197 op_sel_hi:[0,0,0]
	v_mfma_scale_f32_16x16x128_f8f6f4 v[104:107], v[4:11], v[202:209], 0, v117, v197 op_sel_hi:[0,0,0]
	v_mfma_scale_f32_16x16x128_f8f6f4 v[60:63], v[12:19], v[210:217], 0, v117, v197 op_sel_hi:[0,0,0]
	v_mfma_scale_f32_16x16x128_f8f6f4 v[52:55], v[4:11], v[210:217], 0, v117, v197 op_sel_hi:[0,0,0]
	v_mfma_scale_f32_16x16x128_f8f6f4 v[44:47], v[12:19], v[218:225], 0, v117, v197 op_sel_hi:[0,0,0]
	v_mfma_scale_f32_16x16x128_f8f6f4 v[36:39], v[4:11], v[218:225], 0, v117, v197 op_sel_hi:[0,0,0]
	s_setprio 0
	s_barrier
	s_add_u32 s46, s58, 0x20000
	s_addc_u32 s47, s59, 0
	s_add_i32 s6, s6, s64
	v_lshl_add_u64 v[4:5], s[46:47], 0, v[184:185]
	s_mov_b32 m0, s6
	s_nop 0
	global_load_lds_dwordx4 v[4:5], off
	v_lshl_add_u64 v[4:5], s[46:47], 0, v[186:187]
	s_add_i32 m0, s6, 0x2000
	s_nop 0
	global_load_lds_dwordx4 v[4:5], off
	s_waitcnt vmcnt(6)
	s_barrier
	s_setprio 1
	v_mfma_scale_f32_16x16x128_f8f6f4 v[126:129], v[28:35], v[174:181], 0, v117, v197 op_sel_hi:[0,0,0]
	v_mfma_scale_f32_16x16x128_f8f6f4 v[118:121], v[20:27], v[174:181], 0, v117, v197 op_sel_hi:[0,0,0]
	v_mfma_scale_f32_16x16x128_f8f6f4 v[108:111], v[28:35], v[202:209], 0, v117, v197 op_sel_hi:[0,0,0]
	v_mfma_scale_f32_16x16x128_f8f6f4 v[100:103], v[20:27], v[202:209], 0, v117, v197 op_sel_hi:[0,0,0]
	v_mfma_scale_f32_16x16x128_f8f6f4 v[64:67], v[28:35], v[210:217], 0, v117, v197 op_sel_hi:[0,0,0]
	v_mfma_scale_f32_16x16x128_f8f6f4 v[56:59], v[20:27], v[210:217], 0, v117, v197 op_sel_hi:[0,0,0]
	v_mfma_scale_f32_16x16x128_f8f6f4 v[48:51], v[28:35], v[218:225], 0, v117, v197 op_sel_hi:[0,0,0]
	v_mfma_scale_f32_16x16x128_f8f6f4 v[40:43], v[20:27], v[218:225], 0, v117, v197 op_sel_hi:[0,0,0]
	s_setprio 0
	s_add_i32 s6, 0, 0x18400
	v_add_u32_e32 v2, s6, v241
	s_barrier
	ds_read_b128 v[12:15], v2
	ds_read_b128 v[16:19], v2 offset:1024
	ds_read_b128 v[4:7], v2 offset:2048
	ds_read_b128 v[8:11], v2 offset:3072
	s_mov_b32 m0, s68
	v_lshl_add_u64 v[182:183], s[60:61], 0, v[192:193]
	ds_read_b128 v[20:23], v248 offset:33792
	ds_read_b128 v[24:27], v248 offset:34816
	ds_read_b128 v[28:31], v248 offset:35840
	ds_read_b128 v[32:35], v248 offset:36864
	ds_read_b128 v[174:177], v248 offset:37888
	ds_read_b128 v[178:181], v248 offset:38912
	ds_read_b128 v[202:205], v248 offset:39936
	ds_read_b128 v[206:209], v248 offset:40960
	global_load_lds_dwordx4 v[182:183], off
	v_lshl_add_u64 v[182:183], s[60:61], 0, v[194:195]
	s_mov_b32 m0, s69
	s_nop 0
	global_load_lds_dwordx4 v[182:183], off
	s_waitcnt lgkmcnt(8)
	s_barrier
	s_waitcnt lgkmcnt(0)
	s_setprio 1
	s_waitcnt lgkmcnt(0)
	v_mfma_scale_f32_16x16x128_f8f6f4 v[162:165], v[12:19], v[20:27], v[162:165], v117, v197 op_sel_hi:[0,0,0]
	v_mfma_scale_f32_16x16x128_f8f6f4 v[154:157], v[4:11], v[20:27], v[154:157], v117, v197 op_sel_hi:[0,0,0]
	v_mfma_scale_f32_16x16x128_f8f6f4 v[146:149], v[12:19], v[28:35], v[146:149], v117, v197 op_sel_hi:[0,0,0]
	v_mfma_scale_f32_16x16x128_f8f6f4 v[138:141], v[4:11], v[28:35], v[138:141], v117, v197 op_sel_hi:[0,0,0]
	v_mfma_scale_f32_16x16x128_f8f6f4 v[96:99], v[12:19], v[174:181], v[96:99], v117, v197 op_sel_hi:[0,0,0]
	v_mfma_scale_f32_16x16x128_f8f6f4 v[88:91], v[4:11], v[174:181], v[88:91], v117, v197 op_sel_hi:[0,0,0]
	v_mfma_scale_f32_16x16x128_f8f6f4 v[80:83], v[12:19], v[202:209], v[80:83], v117, v197 op_sel_hi:[0,0,0]
	v_mfma_scale_f32_16x16x128_f8f6f4 v[72:75], v[4:11], v[202:209], v[72:75], v117, v197 op_sel_hi:[0,0,0]
	s_setprio 0
	s_barrier
	s_add_i32 s60, 0, 0x1c400
	s_add_i32 s6, s6, s64
	v_add_u32_e32 v2, s60, v241
	v_lshl_add_u64 v[166:167], v[166:167], 0, s[22:23]
	s_mov_b32 m0, s6
	ds_read_b128 v[210:213], v2
	ds_read_b128 v[214:217], v2 offset:1024
	ds_read_b128 v[218:221], v2 offset:2048
	ds_read_b128 v[222:225], v2 offset:3072
	global_load_lds_dwordx4 v[166:167], off
	v_lshl_add_u64 v[166:167], v[168:169], 0, s[22:23]
	s_add_i32 m0, s6, 0x2000
	s_nop 0
	global_load_lds_dwordx4 v[166:167], off
	s_barrier
	s_waitcnt lgkmcnt(0)
	s_setprio 1
	s_waitcnt lgkmcnt(0)
	v_mfma_scale_f32_16x16x128_f8f6f4 v[158:161], v[210:217], v[20:27], v[158:161], v117, v197 op_sel_hi:[0,0,0]
	v_mfma_scale_f32_16x16x128_f8f6f4 v[150:153], v[218:225], v[20:27], v[150:153], v117, v197 op_sel_hi:[0,0,0]
	v_mfma_scale_f32_16x16x128_f8f6f4 v[142:145], v[210:217], v[28:35], v[142:145], v117, v197 op_sel_hi:[0,0,0]
	v_mfma_scale_f32_16x16x128_f8f6f4 v[134:137], v[218:225], v[28:35], v[134:137], v117, v197 op_sel_hi:[0,0,0]
	v_mfma_scale_f32_16x16x128_f8f6f4 v[92:95], v[210:217], v[174:181], v[92:95], v117, v197 op_sel_hi:[0,0,0]
	v_mfma_scale_f32_16x16x128_f8f6f4 v[84:87], v[218:225], v[174:181], v[84:87], v117, v197 op_sel_hi:[0,0,0]
	v_mfma_scale_f32_16x16x128_f8f6f4 v[76:79], v[210:217], v[202:209], v[76:79], v117, v197 op_sel_hi:[0,0,0]
	v_mfma_scale_f32_16x16x128_f8f6f4 v[68:71], v[218:225], v[202:209], v[68:71], v117, v197 op_sel_hi:[0,0,0]
	s_setprio 0
	s_mov_b32 m0, s75
	v_lshl_add_u64 v[166:167], v[170:171], 0, s[22:23]
	s_barrier
	ds_read_b128 v[20:23], v248 offset:50176
	ds_read_b128 v[24:27], v248 offset:51200
	ds_read_b128 v[28:31], v248 offset:52224
	ds_read_b128 v[32:35], v248 offset:53248
	ds_read_b128 v[174:177], v248 offset:54272
	ds_read_b128 v[178:181], v248 offset:55296
	ds_read_b128 v[202:205], v248 offset:56320
	ds_read_b128 v[206:209], v248 offset:57344
	global_load_lds_dwordx4 v[166:167], off
	v_lshl_add_u64 v[166:167], v[172:173], 0, s[22:23]
	s_mov_b32 m0, s76
	s_nop 0
	global_load_lds_dwordx4 v[166:167], off
	s_barrier
	s_waitcnt lgkmcnt(0)
	s_setprio 1
	s_waitcnt lgkmcnt(0)
	v_mfma_scale_f32_16x16x128_f8f6f4 v[130:133], v[12:19], v[20:27], v[130:133], v117, v197 op_sel_hi:[0,0,0]
	v_mfma_scale_f32_16x16x128_f8f6f4 v[122:125], v[4:11], v[20:27], v[122:125], v117, v197 op_sel_hi:[0,0,0]
	v_mfma_scale_f32_16x16x128_f8f6f4 v[112:115], v[12:19], v[28:35], v[112:115], v117, v197 op_sel_hi:[0,0,0]
	v_mfma_scale_f32_16x16x128_f8f6f4 v[104:107], v[4:11], v[28:35], v[104:107], v117, v197 op_sel_hi:[0,0,0]
	v_mfma_scale_f32_16x16x128_f8f6f4 v[60:63], v[12:19], v[174:181], v[60:63], v117, v197 op_sel_hi:[0,0,0]
	v_mfma_scale_f32_16x16x128_f8f6f4 v[52:55], v[4:11], v[174:181], v[52:55], v117, v197 op_sel_hi:[0,0,0]
	v_mfma_scale_f32_16x16x128_f8f6f4 v[44:47], v[12:19], v[202:209], v[44:47], v117, v197 op_sel_hi:[0,0,0]
	v_mfma_scale_f32_16x16x128_f8f6f4 v[36:39], v[4:11], v[202:209], v[36:39], v117, v197 op_sel_hi:[0,0,0]
	s_setprio 0
	s_barrier
	s_add_u32 s46, s58, 0x20080
	s_addc_u32 s47, s59, 0
	s_add_i32 s6, s60, s64
	v_lshl_add_u64 v[4:5], s[46:47], 0, v[184:185]
	s_mov_b32 m0, s6
	s_nop 0
	global_load_lds_dwordx4 v[4:5], off
	v_lshl_add_u64 v[4:5], s[46:47], 0, v[186:187]
	s_add_i32 m0, s6, 0x2000
	s_nop 0
	global_load_lds_dwordx4 v[4:5], off
	s_waitcnt vmcnt(6)
	s_barrier
	s_setprio 1
	v_mfma_scale_f32_16x16x128_f8f6f4 v[126:129], v[210:217], v[20:27], v[126:129], v117, v197 op_sel_hi:[0,0,0]
	v_mfma_scale_f32_16x16x128_f8f6f4 v[118:121], v[218:225], v[20:27], v[118:121], v117, v197 op_sel_hi:[0,0,0]
	v_mfma_scale_f32_16x16x128_f8f6f4 v[108:111], v[210:217], v[28:35], v[108:111], v117, v197 op_sel_hi:[0,0,0]
	v_mfma_scale_f32_16x16x128_f8f6f4 v[100:103], v[218:225], v[28:35], v[100:103], v117, v197 op_sel_hi:[0,0,0]
	v_mfma_scale_f32_16x16x128_f8f6f4 v[64:67], v[210:217], v[174:181], v[64:67], v117, v197 op_sel_hi:[0,0,0]
	v_mfma_scale_f32_16x16x128_f8f6f4 v[56:59], v[218:225], v[174:181], v[56:59], v117, v197 op_sel_hi:[0,0,0]
	v_mfma_scale_f32_16x16x128_f8f6f4 v[48:51], v[210:217], v[202:209], v[48:51], v117, v197 op_sel_hi:[0,0,0]
	v_mfma_scale_f32_16x16x128_f8f6f4 v[40:43], v[218:225], v[202:209], v[40:43], v117, v197 op_sel_hi:[0,0,0]
	s_setprio 0
	s_add_i32 s3, s3, 2
	s_add_u32 s0, s0, 0x100
	s_addc_u32 s1, s1, 0
	s_cmp_gt_u32 s3, 5
	s_mov_b64 s[46:47], s[44:45]
	s_barrier
	s_cbranch_scc0 .LBB0_1044
	s_branch .Lpexit_qb

.Lpexit_qb:
	v_mul_f32_e32 v4, v163, v163
	v_mul_f32_e32 v5, v155, v155
	v_fmac_f32_e32 v4, v162, v162
	v_fmac_f32_e32 v5, v154, v154
	v_fmac_f32_e32 v4, v164, v164
	v_fmac_f32_e32 v5, v156, v156
	v_fmac_f32_e32 v4, v165, v165
	v_fmac_f32_e32 v5, v157, v157
	v_add_f32_e32 v4, v4, v5
	v_mul_f32_e32 v5, v159, v159
	v_fmac_f32_e32 v5, v158, v158
	v_fmac_f32_e32 v5, v160, v160
	v_fmac_f32_e32 v5, v161, v161
	v_add_f32_e32 v4, v4, v5
	v_mul_f32_e32 v5, v151, v151
	v_fmac_f32_e32 v5, v150, v150
	v_fmac_f32_e32 v5, v152, v152
	v_fmac_f32_e32 v5, v153, v153
	v_add_f32_e32 v4, v4, v5
	v_mov_b32_e32 v5, v4
	s_nop 1
	v_permlane16_swap_b32_e32 v4, v5
	v_add_f32_e32 v4, v4, v5
	v_mov_b32_e32 v5, v4
	s_nop 1
	v_permlane32_swap_b32_e32 v4, v5
	v_add_f32_e32 v4, v4, v5
	v_mul_f32_e32 v5, v147, v147
	v_mul_f32_e32 v6, v139, v139
	v_fmac_f32_e32 v5, v146, v146
	v_fmac_f32_e32 v6, v138, v138
	v_fmac_f32_e32 v5, v148, v148
	v_fmac_f32_e32 v6, v140, v140
	v_fmac_f32_e32 v5, v149, v149
	v_fmac_f32_e32 v6, v141, v141
	v_add_f32_e32 v5, v5, v6
	v_mul_f32_e32 v6, v143, v143
	v_fmac_f32_e32 v6, v142, v142
	v_fmac_f32_e32 v6, v144, v144
	v_fmac_f32_e32 v6, v145, v145
	v_add_f32_e32 v5, v5, v6
	v_mul_f32_e32 v6, v135, v135
	v_fmac_f32_e32 v6, v134, v134
	v_fmac_f32_e32 v6, v136, v136
	v_fmac_f32_e32 v6, v137, v137
	v_add_f32_e32 v5, v5, v6
	v_mov_b32_e32 v6, v5
	s_nop 1
	v_permlane16_swap_b32_e32 v5, v6
	v_add_f32_e32 v5, v5, v6
	v_mov_b32_e32 v6, v5
	s_nop 1
	v_permlane32_swap_b32_e32 v5, v6
	v_add_f32_e32 v5, v5, v6
	v_mul_f32_e32 v6, v97, v97
	v_mul_f32_e32 v7, v89, v89
	v_fmac_f32_e32 v6, v96, v96
	v_fmac_f32_e32 v7, v88, v88
	v_fmac_f32_e32 v6, v98, v98
	v_fmac_f32_e32 v7, v90, v90
	v_fmac_f32_e32 v6, v99, v99
	v_fmac_f32_e32 v7, v91, v91
	v_add_f32_e32 v6, v6, v7
	v_mul_f32_e32 v7, v93, v93
	v_fmac_f32_e32 v7, v92, v92
	v_fmac_f32_e32 v7, v94, v94
	v_fmac_f32_e32 v7, v95, v95
	v_add_f32_e32 v6, v6, v7
	v_mul_f32_e32 v7, v85, v85
	v_fmac_f32_e32 v7, v84, v84
	v_fmac_f32_e32 v7, v86, v86
	v_fmac_f32_e32 v7, v87, v87
	v_add_f32_e32 v6, v6, v7
	v_mov_b32_e32 v7, v6
	s_nop 1
	v_permlane16_swap_b32_e32 v6, v7
	v_add_f32_e32 v6, v6, v7
	v_mov_b32_e32 v7, v6
	s_nop 1
	v_permlane32_swap_b32_e32 v6, v7
	v_add_f32_e32 v6, v6, v7
	v_mul_f32_e32 v7, v81, v81
	v_mul_f32_e32 v8, v73, v73
	v_fmac_f32_e32 v7, v80, v80
	v_fmac_f32_e32 v8, v72, v72
	v_fmac_f32_e32 v7, v82, v82
	v_fmac_f32_e32 v8, v74, v74
	v_fmac_f32_e32 v7, v83, v83
	v_fmac_f32_e32 v8, v75, v75
	v_add_f32_e32 v7, v7, v8
	v_mul_f32_e32 v8, v77, v77
	v_fmac_f32_e32 v8, v76, v76
	v_fmac_f32_e32 v8, v78, v78
	v_fmac_f32_e32 v8, v79, v79
	v_add_f32_e32 v7, v7, v8
	v_mul_f32_e32 v8, v69, v69
	v_fmac_f32_e32 v8, v68, v68
	v_fmac_f32_e32 v8, v70, v70
	v_fmac_f32_e32 v8, v71, v71
	v_add_f32_e32 v7, v7, v8
	v_mov_b32_e32 v8, v7
	s_nop 1
	v_permlane16_swap_b32_e32 v7, v8
	v_add_f32_e32 v7, v7, v8
	v_mov_b32_e32 v8, v7
	s_nop 1
	v_permlane32_swap_b32_e32 v7, v8
	v_add_f32_e32 v7, v7, v8
	v_mul_f32_e32 v8, v131, v131
	v_mul_f32_e32 v9, v123, v123
	v_fmac_f32_e32 v8, v130, v130
	v_fmac_f32_e32 v9, v122, v122
	v_fmac_f32_e32 v8, v132, v132
	v_fmac_f32_e32 v9, v124, v124
	v_fmac_f32_e32 v8, v133, v133
	v_fmac_f32_e32 v9, v125, v125
	v_add_f32_e32 v8, v8, v9
	v_mul_f32_e32 v9, v127, v127
	v_fmac_f32_e32 v9, v126, v126
	v_fmac_f32_e32 v9, v128, v128
	v_fmac_f32_e32 v9, v129, v129
	v_add_f32_e32 v8, v8, v9
	v_mul_f32_e32 v9, v119, v119
	v_fmac_f32_e32 v9, v118, v118
	v_fmac_f32_e32 v9, v120, v120
	v_fmac_f32_e32 v9, v121, v121
	v_add_f32_e32 v8, v8, v9
	v_mov_b32_e32 v9, v8
	s_nop 1
	v_permlane16_swap_b32_e32 v8, v9
	v_add_f32_e32 v8, v8, v9
	v_mov_b32_e32 v9, v8
	s_nop 1
	v_permlane32_swap_b32_e32 v8, v9
	v_add_f32_e32 v8, v8, v9
	v_mul_f32_e32 v9, v113, v113
	v_mul_f32_e32 v10, v105, v105
	v_fmac_f32_e32 v9, v112, v112
	v_fmac_f32_e32 v10, v104, v104
	v_fmac_f32_e32 v9, v114, v114
	v_fmac_f32_e32 v10, v106, v106
	v_fmac_f32_e32 v9, v115, v115
	v_fmac_f32_e32 v10, v107, v107
	v_add_f32_e32 v9, v9, v10
	v_mul_f32_e32 v10, v109, v109
	v_fmac_f32_e32 v10, v108, v108
	v_fmac_f32_e32 v10, v110, v110
	v_fmac_f32_e32 v10, v111, v111
	v_add_f32_e32 v9, v9, v10
	v_mul_f32_e32 v10, v101, v101
	v_fmac_f32_e32 v10, v100, v100
	v_fmac_f32_e32 v10, v102, v102
	v_fmac_f32_e32 v10, v103, v103
	v_add_f32_e32 v9, v9, v10
	v_mov_b32_e32 v10, v9
	s_nop 1
	v_permlane16_swap_b32_e32 v9, v10
	v_add_f32_e32 v9, v9, v10
	v_mov_b32_e32 v10, v9
	s_nop 1
	v_permlane32_swap_b32_e32 v9, v10
	v_add_f32_e32 v9, v9, v10
	v_mul_f32_e32 v10, v61, v61
	v_mul_f32_e32 v11, v53, v53
	v_fmac_f32_e32 v10, v60, v60
	v_fmac_f32_e32 v11, v52, v52
	v_fmac_f32_e32 v10, v62, v62
	v_fmac_f32_e32 v11, v54, v54
	v_fmac_f32_e32 v10, v63, v63
	v_fmac_f32_e32 v11, v55, v55
	v_add_f32_e32 v10, v10, v11
	v_mul_f32_e32 v11, v65, v65
	v_fmac_f32_e32 v11, v64, v64
	v_fmac_f32_e32 v11, v66, v66
	v_fmac_f32_e32 v11, v67, v67
	v_add_f32_e32 v10, v10, v11
	v_mul_f32_e32 v11, v57, v57
	v_fmac_f32_e32 v11, v56, v56
	v_fmac_f32_e32 v11, v58, v58
	v_fmac_f32_e32 v11, v59, v59
	v_add_f32_e32 v10, v10, v11
	v_mov_b32_e32 v11, v10
	s_nop 1
	v_permlane16_swap_b32_e32 v10, v11
	v_add_f32_e32 v10, v10, v11
	v_mov_b32_e32 v11, v10
	s_nop 1
	v_permlane32_swap_b32_e32 v10, v11
	v_add_f32_e32 v10, v10, v11
	v_mul_f32_e32 v11, v45, v45
	v_mul_f32_e32 v12, v37, v37
	v_fmac_f32_e32 v11, v44, v44
	v_fmac_f32_e32 v12, v36, v36
	v_fmac_f32_e32 v11, v46, v46
	v_fmac_f32_e32 v12, v38, v38
	v_fmac_f32_e32 v11, v47, v47
	v_fmac_f32_e32 v12, v39, v39
	v_add_f32_e32 v11, v11, v12
	v_mul_f32_e32 v12, v49, v49
	v_fmac_f32_e32 v12, v48, v48
	v_fmac_f32_e32 v12, v50, v50
	v_fmac_f32_e32 v12, v51, v51
	v_add_f32_e32 v11, v11, v12
	v_mul_f32_e32 v12, v41, v41
	v_fmac_f32_e32 v12, v40, v40
	v_fmac_f32_e32 v12, v42, v42
	v_fmac_f32_e32 v12, v43, v43
	v_add_f32_e32 v11, v11, v12
	v_mov_b32_e32 v12, v11
	s_nop 1
	v_permlane16_swap_b32_e32 v11, v12
	v_add_f32_e32 v11, v11, v12
	s_nop 15
	s_nop 15
	v_mov_b32_e32 v12, v11
	s_nop 1
	v_permlane32_swap_b32_e32 v11, v12
	v_mov_b32_e32 v2, v240
	v_add_f32_e32 v11, v11, v12
	s_and_saveexec_b64 s[0:1], s[38:39]
	s_cbranch_execz .LBB0_1047
	v_lshl_add_u32 v12, v2, 2, s82
	ds_write2_b32 v12, v4, v5 offset1:16
	ds_write2_b32 v12, v6, v7 offset0:32 offset1:48
	ds_write2_b32 v12, v8, v9 offset0:64 offset1:80
	ds_write2_b32 v12, v10, v11 offset0:96 offset1:112

.LBB0_1915:
	v_lshl_add_u64 v[4:5], s[36:37], 0, v[172:173]
	global_load_dword v206, v[4:5], off
	s_add_u32 s0, s36, 0x200
	v_lshl_add_u64 v[4:5], s[36:37], 0, v[174:175]
	global_load_dword v207, v[4:5], off
	s_addc_u32 s1, s37, 0
	v_lshl_add_u64 v[4:5], s[0:1], 0, v[172:173]
	global_load_dword v208, v[4:5], off
	s_add_u32 s6, s50, 0x100
	v_lshl_add_u64 v[4:5], s[0:1], 0, v[174:175]
	global_load_dword v209, v[4:5], off
	s_addc_u32 s43, s51, 0
	s_add_u32 s50, s26, 0x80
	v_mov_b32_e32 v179, v3
	v_mov_b32_e32 v177, v3
	s_addc_u32 s51, s27, 0
	s_mov_b32 s45, -2
	s_branch .Lpeelf1_1917

.Lpeelf1_1916:
	s_add_u32 s52, s50, 0x80
	s_addc_u32 s53, s51, 0
	s_and_b64 s[0:1], s[0:1], exec
	s_cselect_b32 s55, s27, s53
	s_cselect_b32 s54, s26, s52
	s_cselect_b32 s53, s47, s43
	s_cselect_b32 s52, s46, s6
	s_add_i32 s1, 0, 0x10400
	v_add_u32_e32 v8, s1, v185
	ds_read_b128 v[12:15], v8
	ds_read_b128 v[16:19], v8 offset:1024
	ds_read_b128 v[4:7], v8 offset:2048
	ds_read_b128 v[8:11], v8 offset:3072
	v_lshl_add_u64 v[20:21], s[50:51], 0, v[178:179]
	s_add_i32 m0, s49, 0xc400
	ds_read_b128 v[210:213], v201 offset:1024
	ds_read_b128 v[214:217], v201 offset:2048
	ds_read_b128 v[218:221], v201 offset:3072
	ds_read_b128 v[222:225], v201 offset:4096
	ds_read_b128 v[230:233], v201 offset:5120
	ds_read_b128 v[234:237], v201 offset:6144
	ds_read_b128 v[240:243], v201 offset:7168
	ds_read_b128 v[244:247], v201 offset:8192
	global_load_lds_dwordx4 v[20:21], off
	v_lshl_add_u64 v[20:21], s[50:51], 0, v[176:177]
	s_add_i32 m0, s49, 0xe400
	s_nop 0
	global_load_lds_dwordx4 v[20:21], off
	s_waitcnt lgkmcnt(8)
	s_barrier
	s_waitcnt lgkmcnt(0)
	s_setprio 1
	s_waitcnt lgkmcnt(0)
	v_mfma_scale_f32_16x16x128_f8f6f4 v[162:165], v[12:19], v[210:217], 0, v117, v198 op_sel_hi:[0,0,0]
	v_mfma_scale_f32_16x16x128_f8f6f4 v[154:157], v[4:11], v[210:217], 0, v117, v198 op_sel_hi:[0,0,0]
	v_mfma_scale_f32_16x16x128_f8f6f4 v[146:149], v[12:19], v[218:225], 0, v117, v198 op_sel_hi:[0,0,0]
	v_mfma_scale_f32_16x16x128_f8f6f4 v[138:141], v[4:11], v[218:225], 0, v117, v198 op_sel_hi:[0,0,0]
	v_mfma_scale_f32_16x16x128_f8f6f4 v[130:133], v[12:19], v[230:237], 0, v117, v198 op_sel_hi:[0,0,0]
	v_mfma_scale_f32_16x16x128_f8f6f4 v[122:125], v[4:11], v[230:237], 0, v117, v198 op_sel_hi:[0,0,0]
	v_mfma_scale_f32_16x16x128_f8f6f4 v[112:115], v[12:19], v[240:247], 0, v117, v198 op_sel_hi:[0,0,0]
	v_mfma_scale_f32_16x16x128_f8f6f4 v[104:107], v[4:11], v[240:247], 0, v117, v198 op_sel_hi:[0,0,0]
	s_setprio 0
	s_barrier
	s_add_i32 s0, 0, 0x14400
	s_add_i32 s1, s1, s56
	v_add_u32_e32 v24, s0, v185
	v_lshl_add_u64 v[190:191], s[52:53], 0, v[168:169]
	s_mov_b32 m0, s1
	ds_read_b128 v[28:31], v24
	ds_read_b128 v[32:35], v24 offset:1024
	ds_read_b128 v[20:23], v24 offset:2048
	ds_read_b128 v[24:27], v24 offset:3072
	global_load_lds_dwordx4 v[190:191], off
	v_lshl_add_u64 v[192:193], s[52:53], 0, v[166:167]
	s_add_i32 m0, s1, 0x2000
	s_nop 0
	global_load_lds_dwordx4 v[192:193], off
	s_barrier
	s_waitcnt lgkmcnt(0)
	s_setprio 1
	s_waitcnt lgkmcnt(0)
	v_mfma_scale_f32_16x16x128_f8f6f4 v[158:161], v[28:35], v[210:217], 0, v117, v198 op_sel_hi:[0,0,0]
	v_mfma_scale_f32_16x16x128_f8f6f4 v[150:153], v[20:27], v[210:217], 0, v117, v198 op_sel_hi:[0,0,0]
	v_mfma_scale_f32_16x16x128_f8f6f4 v[142:145], v[28:35], v[218:225], 0, v117, v198 op_sel_hi:[0,0,0]
	v_mfma_scale_f32_16x16x128_f8f6f4 v[134:137], v[20:27], v[218:225], 0, v117, v198 op_sel_hi:[0,0,0]
	v_mfma_scale_f32_16x16x128_f8f6f4 v[126:129], v[28:35], v[230:237], 0, v117, v198 op_sel_hi:[0,0,0]
	v_mfma_scale_f32_16x16x128_f8f6f4 v[118:121], v[20:27], v[230:237], 0, v117, v198 op_sel_hi:[0,0,0]
	v_mfma_scale_f32_16x16x128_f8f6f4 v[108:111], v[28:35], v[240:247], 0, v117, v198 op_sel_hi:[0,0,0]
	v_mfma_scale_f32_16x16x128_f8f6f4 v[100:103], v[20:27], v[240:247], 0, v117, v198 op_sel_hi:[0,0,0]
	s_setprio 0
	s_mov_b32 m0, s63
	s_barrier
	ds_read_b128 v[210:213], v201 offset:17408
	ds_read_b128 v[214:217], v201 offset:18432
	ds_read_b128 v[218:221], v201 offset:19456
	ds_read_b128 v[222:225], v201 offset:20480
	ds_read_b128 v[230:233], v201 offset:21504
	ds_read_b128 v[234:237], v201 offset:22528
	ds_read_b128 v[240:243], v201 offset:23552
	ds_read_b128 v[244:247], v201 offset:24576
	global_load_lds_dwordx4 v2, s[54:55]
	s_mov_b32 m0, s64
	v_mov_b32_e32 v195, v3
	global_load_lds_dwordx4 v194, s[54:55]
	s_barrier
	s_waitcnt lgkmcnt(0)
	v_lshl_add_u64 v[196:197], s[54:55], 0, v[2:3]
	v_lshl_add_u64 v[194:195], s[54:55], 0, v[194:195]
	s_setprio 1
	s_waitcnt lgkmcnt(0)
	v_mfma_scale_f32_16x16x128_f8f6f4 v[96:99], v[12:19], v[210:217], 0, v117, v198 op_sel_hi:[0,0,0]
	v_mfma_scale_f32_16x16x128_f8f6f4 v[88:91], v[4:11], v[210:217], 0, v117, v198 op_sel_hi:[0,0,0]
	v_mfma_scale_f32_16x16x128_f8f6f4 v[80:83], v[12:19], v[218:225], 0, v117, v198 op_sel_hi:[0,0,0]
	v_mfma_scale_f32_16x16x128_f8f6f4 v[72:75], v[4:11], v[218:225], 0, v117, v198 op_sel_hi:[0,0,0]
	v_mfma_scale_f32_16x16x128_f8f6f4 v[60:63], v[12:19], v[230:237], 0, v117, v198 op_sel_hi:[0,0,0]
	v_mfma_scale_f32_16x16x128_f8f6f4 v[52:55], v[4:11], v[230:237], 0, v117, v198 op_sel_hi:[0,0,0]
	v_mfma_scale_f32_16x16x128_f8f6f4 v[44:47], v[12:19], v[240:247], 0, v117, v198 op_sel_hi:[0,0,0]
	v_mfma_scale_f32_16x16x128_f8f6f4 v[36:39], v[4:11], v[240:247], 0, v117, v198 op_sel_hi:[0,0,0]
	s_setprio 0
	s_barrier
	s_add_u32 s70, s52, 0x20000
	s_addc_u32 s71, s53, 0
	s_add_i32 s0, s0, s56
	v_lshl_add_u64 v[4:5], s[70:71], 0, v[168:169]
	s_mov_b32 m0, s0
	s_nop 0
	global_load_lds_dwordx4 v[4:5], off
	v_lshl_add_u64 v[4:5], s[70:71], 0, v[166:167]
	s_add_i32 m0, s0, 0x2000
	s_nop 0
	global_load_lds_dwordx4 v[4:5], off
	s_waitcnt vmcnt(6)
	s_barrier
	s_setprio 1
	v_mfma_scale_f32_16x16x128_f8f6f4 v[92:95], v[28:35], v[210:217], 0, v117, v198 op_sel_hi:[0,0,0]
	v_mfma_scale_f32_16x16x128_f8f6f4 v[84:87], v[20:27], v[210:217], 0, v117, v198 op_sel_hi:[0,0,0]
	v_mfma_scale_f32_16x16x128_f8f6f4 v[76:79], v[28:35], v[218:225], 0, v117, v198 op_sel_hi:[0,0,0]
	v_mfma_scale_f32_16x16x128_f8f6f4 v[68:71], v[20:27], v[218:225], 0, v117, v198 op_sel_hi:[0,0,0]
	v_mfma_scale_f32_16x16x128_f8f6f4 v[64:67], v[28:35], v[230:237], 0, v117, v198 op_sel_hi:[0,0,0]
	v_mfma_scale_f32_16x16x128_f8f6f4 v[56:59], v[20:27], v[230:237], 0, v117, v198 op_sel_hi:[0,0,0]
	v_mfma_scale_f32_16x16x128_f8f6f4 v[48:51], v[28:35], v[240:247], 0, v117, v198 op_sel_hi:[0,0,0]
	v_mfma_scale_f32_16x16x128_f8f6f4 v[40:43], v[20:27], v[240:247], 0, v117, v198 op_sel_hi:[0,0,0]
	s_setprio 0
	s_add_i32 s0, 0, 0x18400
	v_add_u32_e32 v2, s0, v185
	s_barrier
	ds_read_b128 v[12:15], v2
	ds_read_b128 v[16:19], v2 offset:1024
	ds_read_b128 v[4:7], v2 offset:2048
	ds_read_b128 v[8:11], v2 offset:3072
	s_mov_b32 m0, s65
	v_lshl_add_u64 v[182:183], s[54:55], 0, v[188:189]
	ds_read_b128 v[20:23], v201 offset:33792
	ds_read_b128 v[24:27], v201 offset:34816
	ds_read_b128 v[28:31], v201 offset:35840
	ds_read_b128 v[32:35], v201 offset:36864
	ds_read_b128 v[210:213], v201 offset:37888
	ds_read_b128 v[214:217], v201 offset:38912
	ds_read_b128 v[218:221], v201 offset:39936
	ds_read_b128 v[222:225], v201 offset:40960
	global_load_lds_dwordx4 v[182:183], off
	v_lshl_add_u64 v[182:183], s[54:55], 0, v[186:187]
	s_mov_b32 m0, s66
	s_nop 0
	global_load_lds_dwordx4 v[182:183], off
	s_waitcnt lgkmcnt(8)
	s_barrier
	s_waitcnt lgkmcnt(0)
	s_setprio 1
	s_waitcnt lgkmcnt(0)
	v_mfma_scale_f32_16x16x128_f8f6f4 v[162:165], v[12:19], v[20:27], v[162:165], v117, v198 op_sel_hi:[0,0,0]
	v_mfma_scale_f32_16x16x128_f8f6f4 v[154:157], v[4:11], v[20:27], v[154:157], v117, v198 op_sel_hi:[0,0,0]
	v_mfma_scale_f32_16x16x128_f8f6f4 v[146:149], v[12:19], v[28:35], v[146:149], v117, v198 op_sel_hi:[0,0,0]
	v_mfma_scale_f32_16x16x128_f8f6f4 v[138:141], v[4:11], v[28:35], v[138:141], v117, v198 op_sel_hi:[0,0,0]
	v_mfma_scale_f32_16x16x128_f8f6f4 v[130:133], v[12:19], v[210:217], v[130:133], v117, v198 op_sel_hi:[0,0,0]
	v_mfma_scale_f32_16x16x128_f8f6f4 v[122:125], v[4:11], v[210:217], v[122:125], v117, v198 op_sel_hi:[0,0,0]
	v_mfma_scale_f32_16x16x128_f8f6f4 v[112:115], v[12:19], v[218:225], v[112:115], v117, v198 op_sel_hi:[0,0,0]
	v_mfma_scale_f32_16x16x128_f8f6f4 v[104:107], v[4:11], v[218:225], v[104:107], v117, v198 op_sel_hi:[0,0,0]
	s_setprio 0
	s_barrier
	s_add_i32 s54, 0, 0x1c400
	s_add_i32 s0, s0, s56
	v_add_u32_e32 v2, s54, v185
	v_lshl_add_u64 v[182:183], v[190:191], 0, s[22:23]
	s_mov_b32 m0, s0
	ds_read_b128 v[230:233], v2
	ds_read_b128 v[234:237], v2 offset:1024
	ds_read_b128 v[240:243], v2 offset:2048
	ds_read_b128 v[244:247], v2 offset:3072
	global_load_lds_dwordx4 v[182:183], off
	v_lshl_add_u64 v[182:183], v[192:193], 0, s[22:23]
	s_add_i32 m0, s0, 0x2000
	s_nop 0
	global_load_lds_dwordx4 v[182:183], off
	s_barrier
	s_waitcnt lgkmcnt(0)
	s_setprio 1
	s_waitcnt lgkmcnt(0)
	v_mfma_scale_f32_16x16x128_f8f6f4 v[158:161], v[230:237], v[20:27], v[158:161], v117, v198 op_sel_hi:[0,0,0]
	v_mfma_scale_f32_16x16x128_f8f6f4 v[150:153], v[240:247], v[20:27], v[150:153], v117, v198 op_sel_hi:[0,0,0]
	v_mfma_scale_f32_16x16x128_f8f6f4 v[142:145], v[230:237], v[28:35], v[142:145], v117, v198 op_sel_hi:[0,0,0]
	v_mfma_scale_f32_16x16x128_f8f6f4 v[134:137], v[240:247], v[28:35], v[134:137], v117, v198 op_sel_hi:[0,0,0]
	v_mfma_scale_f32_16x16x128_f8f6f4 v[126:129], v[230:237], v[210:217], v[126:129], v117, v198 op_sel_hi:[0,0,0]
	v_mfma_scale_f32_16x16x128_f8f6f4 v[118:121], v[240:247], v[210:217], v[118:121], v117, v198 op_sel_hi:[0,0,0]
	v_mfma_scale_f32_16x16x128_f8f6f4 v[108:111], v[230:237], v[218:225], v[108:111], v117, v198 op_sel_hi:[0,0,0]
	v_mfma_scale_f32_16x16x128_f8f6f4 v[100:103], v[240:247], v[218:225], v[100:103], v117, v198 op_sel_hi:[0,0,0]
	s_setprio 0
	s_mov_b32 m0, s67
	v_lshl_add_u64 v[182:183], v[196:197], 0, s[22:23]
	s_barrier
	ds_read_b128 v[20:23], v201 offset:50176
	ds_read_b128 v[24:27], v201 offset:51200
	ds_read_b128 v[28:31], v201 offset:52224
	ds_read_b128 v[32:35], v201 offset:53248
	ds_read_b128 v[186:189], v201 offset:54272
	ds_read_b128 v[190:193], v201 offset:55296
	ds_read_b128 v[210:213], v201 offset:56320
	ds_read_b128 v[214:217], v201 offset:57344
	global_load_lds_dwordx4 v[182:183], off
	v_lshl_add_u64 v[182:183], v[194:195], 0, s[22:23]
	s_mov_b32 m0, s68
	s_nop 0
	global_load_lds_dwordx4 v[182:183], off
	s_barrier
	s_waitcnt lgkmcnt(0)
	s_setprio 1
	s_waitcnt lgkmcnt(0)
	v_mfma_scale_f32_16x16x128_f8f6f4 v[96:99], v[12:19], v[20:27], v[96:99], v117, v198 op_sel_hi:[0,0,0]
	v_mfma_scale_f32_16x16x128_f8f6f4 v[88:91], v[4:11], v[20:27], v[88:91], v117, v198 op_sel_hi:[0,0,0]
	v_mfma_scale_f32_16x16x128_f8f6f4 v[80:83], v[12:19], v[28:35], v[80:83], v117, v198 op_sel_hi:[0,0,0]
	v_mfma_scale_f32_16x16x128_f8f6f4 v[72:75], v[4:11], v[28:35], v[72:75], v117, v198 op_sel_hi:[0,0,0]
	v_mfma_scale_f32_16x16x128_f8f6f4 v[60:63], v[12:19], v[186:193], v[60:63], v117, v198 op_sel_hi:[0,0,0]
	v_mfma_scale_f32_16x16x128_f8f6f4 v[52:55], v[4:11], v[186:193], v[52:55], v117, v198 op_sel_hi:[0,0,0]
	v_mfma_scale_f32_16x16x128_f8f6f4 v[44:47], v[12:19], v[210:217], v[44:47], v117, v198 op_sel_hi:[0,0,0]
	v_mfma_scale_f32_16x16x128_f8f6f4 v[36:39], v[4:11], v[210:217], v[36:39], v117, v198 op_sel_hi:[0,0,0]
	s_setprio 0
	s_barrier
	s_add_u32 s0, s52, 0x20080
	s_addc_u32 s1, s53, 0
	s_add_i32 s52, s54, s56
	v_lshl_add_u64 v[4:5], s[0:1], 0, v[168:169]
	s_mov_b32 m0, s52
	s_nop 0
	global_load_lds_dwordx4 v[4:5], off
	v_lshl_add_u64 v[4:5], s[0:1], 0, v[166:167]
	s_add_i32 m0, s52, 0x2000
	s_nop 0
	global_load_lds_dwordx4 v[4:5], off
	s_waitcnt vmcnt(6)
	s_barrier
	s_setprio 1
	v_mfma_scale_f32_16x16x128_f8f6f4 v[92:95], v[230:237], v[20:27], v[92:95], v117, v198 op_sel_hi:[0,0,0]
	v_mfma_scale_f32_16x16x128_f8f6f4 v[84:87], v[240:247], v[20:27], v[84:87], v117, v198 op_sel_hi:[0,0,0]
	v_mfma_scale_f32_16x16x128_f8f6f4 v[76:79], v[230:237], v[28:35], v[76:79], v117, v198 op_sel_hi:[0,0,0]
	v_mfma_scale_f32_16x16x128_f8f6f4 v[68:71], v[240:247], v[28:35], v[68:71], v117, v198 op_sel_hi:[0,0,0]
	v_mfma_scale_f32_16x16x128_f8f6f4 v[64:67], v[230:237], v[186:193], v[64:67], v117, v198 op_sel_hi:[0,0,0]
	v_mfma_scale_f32_16x16x128_f8f6f4 v[56:59], v[240:247], v[186:193], v[56:59], v117, v198 op_sel_hi:[0,0,0]
	v_mfma_scale_f32_16x16x128_f8f6f4 v[48:51], v[230:237], v[210:217], v[48:51], v117, v198 op_sel_hi:[0,0,0]
	v_mfma_scale_f32_16x16x128_f8f6f4 v[40:43], v[240:247], v[210:217], v[40:43], v117, v198 op_sel_hi:[0,0,0]
	s_setprio 0
	s_add_i32 s45, s45, 2
	s_add_u32 s6, s6, 0x100
	s_addc_u32 s43, s43, 0
	s_add_u32 s50, s50, 0x100
	s_addc_u32 s51, s51, 0
	s_cmp_gt_u32 s45, 5
	s_barrier
	s_cbranch_scc1 .LBB0_1912
	s_branch .LBB0_1917

.LBB0_1983:
	v_lshl_add_u32 v200, s58, 8, v187
	v_ashrrev_i32_e32 v201, 31, v200
	v_lshl_add_u64 v[4:5], v[200:201], 2, s[44:45]
	global_load_dword v198, v[4:5], off
	v_lshl_add_u64 v[6:7], v[4:5], 0, 64
	global_load_dword v196, v[6:7], off
	v_lshl_add_u64 v[6:7], v[4:5], 0, s[22:23]
	s_mov_b64 s[0:1], 0xc0
	global_load_dword v194, v[6:7], off
	v_lshl_add_u64 v[6:7], v[4:5], 0, s[0:1]
	s_mov_b64 s[0:1], 0x200
	global_load_dword v192, v[6:7], off
	v_lshl_add_u64 v[6:7], v[4:5], 0, s[0:1]
	s_mov_b64 s[0:1], 0x240
	global_load_dword v190, v[6:7], off
	v_lshl_add_u64 v[6:7], v[4:5], 0, s[0:1]
	s_mov_b64 s[0:1], 0x280
	global_load_dword v188, v[6:7], off
	v_lshl_add_u64 v[6:7], v[4:5], 0, s[0:1]
	s_mov_b64 s[0:1], 0x2c0
	global_load_dword v186, v[6:7], off
	v_lshl_add_u64 v[4:5], v[4:5], 0, s[0:1]
	s_add_u32 s0, s56, 0x100
	global_load_dword v184, v[4:5], off
	s_addc_u32 s1, s57, 0
	s_add_u32 s54, s54, 0x80
	s_addc_u32 s55, s55, 0
	s_mov_b32 s47, -2
.Lpeelf2_hdr:
	s_add_u32 s49, s54, 0x80
	s_addc_u32 s56, s55, 0
	s_cmp_eq_u32 s47, 12
	s_cselect_b32 s59, s51, s56
	s_cselect_b32 s58, s50, s49
	s_cselect_b32 s57, s53, s1
	s_cselect_b32 s56, s52, s0
	s_add_i32 s78, 0, 0x10400
	v_add_u32_e32 v8, s78, v189
	ds_read_b128 v[12:15], v8
	ds_read_b128 v[16:19], v8 offset:1024
	ds_read_b128 v[4:7], v8 offset:2048
	ds_read_b128 v[8:11], v8 offset:3072
	v_lshl_add_u64 v[20:21], s[54:55], 0, v[180:181]
	s_add_i32 m0, s68, 0xc400
	ds_read_b128 v[206:209], v191 offset:1024
	ds_read_b128 v[210:213], v191 offset:2048
	ds_read_b128 v[214:217], v191 offset:3072
	ds_read_b128 v[218:221], v191 offset:4096
	ds_read_b128 v[230:233], v191 offset:5120
	ds_read_b128 v[234:237], v191 offset:6144
	ds_read_b128 v[240:243], v191 offset:7168
	ds_read_b128 v[244:247], v191 offset:8192
	global_load_lds_dwordx4 v[20:21], off
	v_lshl_add_u64 v[20:21], s[54:55], 0, v[178:179]
	s_add_i32 m0, s68, 0xe400
	s_nop 0
	global_load_lds_dwordx4 v[20:21], off
	s_waitcnt lgkmcnt(8)
	s_barrier
	s_waitcnt lgkmcnt(0)
	s_setprio 1
	s_waitcnt lgkmcnt(0)
	v_mfma_scale_f32_16x16x128_f8f6f4 v[162:165], v[12:19], v[206:213], 0, v117, v185 op_sel_hi:[0,0,0]
	v_mfma_scale_f32_16x16x128_f8f6f4 v[158:161], v[4:11], v[206:213], 0, v117, v185 op_sel_hi:[0,0,0]
	v_mfma_scale_f32_16x16x128_f8f6f4 v[154:157], v[12:19], v[214:221], 0, v117, v185 op_sel_hi:[0,0,0]
	v_mfma_scale_f32_16x16x128_f8f6f4 v[146:149], v[4:11], v[214:221], 0, v117, v185 op_sel_hi:[0,0,0]
	v_mfma_scale_f32_16x16x128_f8f6f4 v[138:141], v[12:19], v[230:237], 0, v117, v185 op_sel_hi:[0,0,0]
	v_mfma_scale_f32_16x16x128_f8f6f4 v[130:133], v[4:11], v[230:237], 0, v117, v185 op_sel_hi:[0,0,0]
	v_mfma_scale_f32_16x16x128_f8f6f4 v[122:125], v[12:19], v[240:247], 0, v117, v185 op_sel_hi:[0,0,0]
	v_mfma_scale_f32_16x16x128_f8f6f4 v[112:115], v[4:11], v[240:247], 0, v117, v185 op_sel_hi:[0,0,0]
	s_setprio 0
	s_barrier
	s_add_i32 s49, 0, 0x14400
	s_add_i32 s78, s78, s63
	v_add_u32_e32 v24, s49, v189
	v_lshl_add_u64 v[202:203], s[56:57], 0, v[168:169]
	s_mov_b32 m0, s78
	ds_read_b128 v[28:31], v24
	ds_read_b128 v[32:35], v24 offset:1024
	ds_read_b128 v[20:23], v24 offset:2048
	ds_read_b128 v[24:27], v24 offset:3072
	global_load_lds_dwordx4 v[202:203], off
	v_lshl_add_u64 v[204:205], s[56:57], 0, v[166:167]
	s_add_i32 m0, s78, 0x2000
	s_nop 0
	global_load_lds_dwordx4 v[204:205], off
	s_barrier
	s_waitcnt lgkmcnt(0)
	s_setprio 1
	s_waitcnt lgkmcnt(0)
	v_mfma_scale_f32_16x16x128_f8f6f4 v[150:153], v[28:35], v[206:213], 0, v117, v185 op_sel_hi:[0,0,0]
	v_mfma_scale_f32_16x16x128_f8f6f4 v[142:145], v[20:27], v[206:213], 0, v117, v185 op_sel_hi:[0,0,0]
	v_mfma_scale_f32_16x16x128_f8f6f4 v[134:137], v[28:35], v[214:221], 0, v117, v185 op_sel_hi:[0,0,0]
	v_mfma_scale_f32_16x16x128_f8f6f4 v[126:129], v[20:27], v[214:221], 0, v117, v185 op_sel_hi:[0,0,0]
	v_mfma_scale_f32_16x16x128_f8f6f4 v[118:121], v[28:35], v[230:237], 0, v117, v185 op_sel_hi:[0,0,0]
	v_mfma_scale_f32_16x16x128_f8f6f4 v[108:111], v[20:27], v[230:237], 0, v117, v185 op_sel_hi:[0,0,0]
	v_mfma_scale_f32_16x16x128_f8f6f4 v[104:107], v[28:35], v[240:247], 0, v117, v185 op_sel_hi:[0,0,0]
	v_mfma_scale_f32_16x16x128_f8f6f4 v[100:103], v[20:27], v[240:247], 0, v117, v185 op_sel_hi:[0,0,0]
	s_setprio 0
	s_mov_b32 m0, s3
	v_lshl_add_u64 v[206:207], s[58:59], 0, v[170:171]
	s_barrier
	ds_read_b128 v[210:213], v191 offset:17408
	ds_read_b128 v[214:217], v191 offset:18432
	ds_read_b128 v[218:221], v191 offset:19456
	ds_read_b128 v[222:225], v191 offset:20480
	ds_read_b128 v[230:233], v191 offset:21504
	ds_read_b128 v[234:237], v191 offset:22528
	ds_read_b128 v[240:243], v191 offset:23552
	ds_read_b128 v[244:247], v191 offset:24576
	global_load_lds_dwordx4 v[206:207], off
	v_lshl_add_u64 v[208:209], s[58:59], 0, v[172:173]
	s_mov_b32 m0, s69
	s_nop 0
	global_load_lds_dwordx4 v[208:209], off
	s_barrier
	s_waitcnt lgkmcnt(0)
	s_setprio 1
	s_waitcnt lgkmcnt(0)
	v_mfma_scale_f32_16x16x128_f8f6f4 v[96:99], v[12:19], v[210:217], 0, v117, v185 op_sel_hi:[0,0,0]
	v_mfma_scale_f32_16x16x128_f8f6f4 v[92:95], v[4:11], v[210:217], 0, v117, v185 op_sel_hi:[0,0,0]
	v_mfma_scale_f32_16x16x128_f8f6f4 v[80:83], v[12:19], v[218:225], 0, v117, v185 op_sel_hi:[0,0,0]
	v_mfma_scale_f32_16x16x128_f8f6f4 v[72:75], v[4:11], v[218:225], 0, v117, v185 op_sel_hi:[0,0,0]
	v_mfma_scale_f32_16x16x128_f8f6f4 v[56:59], v[12:19], v[230:237], 0, v117, v185 op_sel_hi:[0,0,0]
	v_mfma_scale_f32_16x16x128_f8f6f4 v[48:51], v[4:11], v[230:237], 0, v117, v185 op_sel_hi:[0,0,0]
	v_mfma_scale_f32_16x16x128_f8f6f4 v[40:43], v[12:19], v[240:247], 0, v117, v185 op_sel_hi:[0,0,0]
	v_mfma_scale_f32_16x16x128_f8f6f4 v[36:39], v[4:11], v[240:247], 0, v117, v185 op_sel_hi:[0,0,0]
	s_setprio 0
	s_barrier
	s_add_u32 s78, s56, 0x40000
	s_addc_u32 s79, s57, 0
	s_add_i32 s49, s49, s63
	v_lshl_add_u64 v[4:5], s[78:79], 0, v[168:169]
	s_mov_b32 m0, s49
	s_nop 0
	global_load_lds_dwordx4 v[4:5], off
	v_lshl_add_u64 v[4:5], s[78:79], 0, v[166:167]
	s_add_i32 m0, s49, 0x2000
	s_nop 0
	global_load_lds_dwordx4 v[4:5], off
	s_waitcnt vmcnt(6)
	s_barrier
	s_setprio 1
	v_mfma_scale_f32_16x16x128_f8f6f4 v[76:79], v[28:35], v[210:217], 0, v117, v185 op_sel_hi:[0,0,0]
	v_mfma_scale_f32_16x16x128_f8f6f4 v[68:71], v[20:27], v[210:217], 0, v117, v185 op_sel_hi:[0,0,0]
	v_mfma_scale_f32_16x16x128_f8f6f4 v[52:55], v[28:35], v[218:225], 0, v117, v185 op_sel_hi:[0,0,0]
	v_mfma_scale_f32_16x16x128_f8f6f4 v[44:47], v[20:27], v[218:225], 0, v117, v185 op_sel_hi:[0,0,0]
	v_mfma_scale_f32_16x16x128_f8f6f4 v[88:91], v[28:35], v[230:237], 0, v117, v185 op_sel_hi:[0,0,0]
	v_mfma_scale_f32_16x16x128_f8f6f4 v[84:87], v[20:27], v[230:237], 0, v117, v185 op_sel_hi:[0,0,0]
	v_mfma_scale_f32_16x16x128_f8f6f4 v[64:67], v[28:35], v[240:247], 0, v117, v185 op_sel_hi:[0,0,0]
	v_mfma_scale_f32_16x16x128_f8f6f4 v[60:63], v[20:27], v[240:247], 0, v117, v185 op_sel_hi:[0,0,0]
	s_setprio 0
	s_add_i32 s49, 0, 0x18400
	v_add_u32_e32 v8, s49, v189
	s_barrier
	ds_read_b128 v[12:15], v8
	ds_read_b128 v[16:19], v8 offset:1024
	ds_read_b128 v[4:7], v8 offset:2048
	ds_read_b128 v[8:11], v8 offset:3072
	s_mov_b32 m0, s70
	v_lshl_add_u64 v[182:183], s[58:59], 0, v[174:175]
	ds_read_b128 v[20:23], v191 offset:33792
	ds_read_b128 v[24:27], v191 offset:34816
	ds_read_b128 v[28:31], v191 offset:35840
	ds_read_b128 v[32:35], v191 offset:36864
	ds_read_b128 v[210:213], v191 offset:37888
	ds_read_b128 v[214:217], v191 offset:38912
	ds_read_b128 v[218:221], v191 offset:39936
	ds_read_b128 v[222:225], v191 offset:40960
	global_load_lds_dwordx4 v[182:183], off
	v_lshl_add_u64 v[182:183], s[58:59], 0, v[176:177]
	s_mov_b32 m0, s71
	s_nop 0
	global_load_lds_dwordx4 v[182:183], off
	s_waitcnt lgkmcnt(8)
	s_barrier
	s_waitcnt lgkmcnt(0)
	s_setprio 1
	s_waitcnt lgkmcnt(0)
	v_mfma_scale_f32_16x16x128_f8f6f4 v[162:165], v[12:19], v[20:27], v[162:165], v117, v185 op_sel_hi:[0,0,0]
	v_mfma_scale_f32_16x16x128_f8f6f4 v[158:161], v[4:11], v[20:27], v[158:161], v117, v185 op_sel_hi:[0,0,0]
	v_mfma_scale_f32_16x16x128_f8f6f4 v[154:157], v[12:19], v[28:35], v[154:157], v117, v185 op_sel_hi:[0,0,0]
	v_mfma_scale_f32_16x16x128_f8f6f4 v[146:149], v[4:11], v[28:35], v[146:149], v117, v185 op_sel_hi:[0,0,0]
	v_mfma_scale_f32_16x16x128_f8f6f4 v[138:141], v[12:19], v[210:217], v[138:141], v117, v185 op_sel_hi:[0,0,0]
	v_mfma_scale_f32_16x16x128_f8f6f4 v[130:133], v[4:11], v[210:217], v[130:133], v117, v185 op_sel_hi:[0,0,0]
	v_mfma_scale_f32_16x16x128_f8f6f4 v[122:125], v[12:19], v[218:225], v[122:125], v117, v185 op_sel_hi:[0,0,0]
	v_mfma_scale_f32_16x16x128_f8f6f4 v[112:115], v[4:11], v[218:225], v[112:115], v117, v185 op_sel_hi:[0,0,0]
	s_setprio 0
	s_barrier
	s_add_i32 s58, 0, 0x1c400
	v_add_u32_e32 v182, s58, v189
	s_add_i32 s49, s49, s63
	ds_read_b128 v[230:233], v182
	ds_read_b128 v[234:237], v182 offset:1024
	ds_read_b128 v[240:243], v182 offset:2048
	ds_read_b128 v[244:247], v182 offset:3072
	v_lshl_add_u64 v[182:183], v[202:203], 0, s[22:23]
	s_mov_b32 m0, s49
	s_nop 0
	global_load_lds_dwordx4 v[182:183], off
	v_lshl_add_u64 v[182:183], v[204:205], 0, s[22:23]
	s_add_i32 m0, s49, 0x2000
	s_nop 0
	global_load_lds_dwordx4 v[182:183], off
	s_barrier
	s_waitcnt lgkmcnt(0)
	s_setprio 1
	s_waitcnt lgkmcnt(0)
	v_mfma_scale_f32_16x16x128_f8f6f4 v[150:153], v[230:237], v[20:27], v[150:153], v117, v185 op_sel_hi:[0,0,0]
	v_mfma_scale_f32_16x16x128_f8f6f4 v[142:145], v[240:247], v[20:27], v[142:145], v117, v185 op_sel_hi:[0,0,0]
	v_mfma_scale_f32_16x16x128_f8f6f4 v[134:137], v[230:237], v[28:35], v[134:137], v117, v185 op_sel_hi:[0,0,0]
	v_mfma_scale_f32_16x16x128_f8f6f4 v[126:129], v[240:247], v[28:35], v[126:129], v117, v185 op_sel_hi:[0,0,0]
	v_mfma_scale_f32_16x16x128_f8f6f4 v[118:121], v[230:237], v[210:217], v[118:121], v117, v185 op_sel_hi:[0,0,0]
	v_mfma_scale_f32_16x16x128_f8f6f4 v[108:111], v[240:247], v[210:217], v[108:111], v117, v185 op_sel_hi:[0,0,0]
	v_mfma_scale_f32_16x16x128_f8f6f4 v[104:107], v[230:237], v[218:225], v[104:107], v117, v185 op_sel_hi:[0,0,0]
	v_mfma_scale_f32_16x16x128_f8f6f4 v[100:103], v[240:247], v[218:225], v[100:103], v117, v185 op_sel_hi:[0,0,0]
	s_setprio 0
	s_mov_b32 m0, s72
	v_lshl_add_u64 v[182:183], v[206:207], 0, s[22:23]
	s_barrier
	ds_read_b128 v[20:23], v191 offset:50176
	ds_read_b128 v[24:27], v191 offset:51200
	ds_read_b128 v[28:31], v191 offset:52224
	ds_read_b128 v[32:35], v191 offset:53248
	ds_read_b128 v[210:213], v191 offset:54272
	ds_read_b128 v[214:217], v191 offset:55296
	ds_read_b128 v[218:221], v191 offset:56320
	ds_read_b128 v[222:225], v191 offset:57344
	global_load_lds_dwordx4 v[182:183], off
	v_lshl_add_u64 v[182:183], v[208:209], 0, s[22:23]
	s_mov_b32 m0, s73
	s_nop 0
	global_load_lds_dwordx4 v[182:183], off
	s_barrier
	s_waitcnt lgkmcnt(0)
	s_setprio 1
	s_waitcnt lgkmcnt(0)
	v_mfma_scale_f32_16x16x128_f8f6f4 v[96:99], v[12:19], v[20:27], v[96:99], v117, v185 op_sel_hi:[0,0,0]
	v_mfma_scale_f32_16x16x128_f8f6f4 v[92:95], v[4:11], v[20:27], v[92:95], v117, v185 op_sel_hi:[0,0,0]
	v_mfma_scale_f32_16x16x128_f8f6f4 v[80:83], v[12:19], v[28:35], v[80:83], v117, v185 op_sel_hi:[0,0,0]
	v_mfma_scale_f32_16x16x128_f8f6f4 v[72:75], v[4:11], v[28:35], v[72:75], v117, v185 op_sel_hi:[0,0,0]
	v_mfma_scale_f32_16x16x128_f8f6f4 v[56:59], v[12:19], v[210:217], v[56:59], v117, v185 op_sel_hi:[0,0,0]
	v_mfma_scale_f32_16x16x128_f8f6f4 v[48:51], v[4:11], v[210:217], v[48:51], v117, v185 op_sel_hi:[0,0,0]
	v_mfma_scale_f32_16x16x128_f8f6f4 v[40:43], v[12:19], v[218:225], v[40:43], v117, v185 op_sel_hi:[0,0,0]
	v_mfma_scale_f32_16x16x128_f8f6f4 v[36:39], v[4:11], v[218:225], v[36:39], v117, v185 op_sel_hi:[0,0,0]
	s_setprio 0
	s_barrier
	s_add_u32 s56, s56, 0x40080
	s_addc_u32 s57, s57, 0
	s_add_i32 s49, s58, s63
	v_lshl_add_u64 v[4:5], s[56:57], 0, v[168:169]
	s_mov_b32 m0, s49
	s_nop 0
	global_load_lds_dwordx4 v[4:5], off
	v_lshl_add_u64 v[4:5], s[56:57], 0, v[166:167]
	s_add_i32 m0, s49, 0x2000
	s_nop 0
	global_load_lds_dwordx4 v[4:5], off
	s_waitcnt vmcnt(6)
	s_barrier
	s_setprio 1
	v_mfma_scale_f32_16x16x128_f8f6f4 v[76:79], v[230:237], v[20:27], v[76:79], v117, v185 op_sel_hi:[0,0,0]
	v_mfma_scale_f32_16x16x128_f8f6f4 v[68:71], v[240:247], v[20:27], v[68:71], v117, v185 op_sel_hi:[0,0,0]
	v_mfma_scale_f32_16x16x128_f8f6f4 v[52:55], v[230:237], v[28:35], v[52:55], v117, v185 op_sel_hi:[0,0,0]
	v_mfma_scale_f32_16x16x128_f8f6f4 v[44:47], v[240:247], v[28:35], v[44:47], v117, v185 op_sel_hi:[0,0,0]
	v_mfma_scale_f32_16x16x128_f8f6f4 v[88:91], v[230:237], v[210:217], v[88:91], v117, v185 op_sel_hi:[0,0,0]
	v_mfma_scale_f32_16x16x128_f8f6f4 v[84:87], v[240:247], v[210:217], v[84:87], v117, v185 op_sel_hi:[0,0,0]
	v_mfma_scale_f32_16x16x128_f8f6f4 v[64:67], v[230:237], v[218:225], v[64:67], v117, v185 op_sel_hi:[0,0,0]
	v_mfma_scale_f32_16x16x128_f8f6f4 v[60:63], v[240:247], v[218:225], v[60:63], v117, v185 op_sel_hi:[0,0,0]
	s_setprio 0
	s_add_i32 s47, s47, 2
	s_add_u32 s0, s0, 0x100
	s_addc_u32 s1, s1, 0
	s_add_u32 s54, s54, 0x100
	s_addc_u32 s55, s55, 0
	s_cmp_gt_u32 s47, 13
	s_barrier
	s_cbranch_scc0 .LBB0_1984
	s_branch .Lpexit_f2

.Lpexit_f2:
	v_lshlrev_b64 v[4:5], 11, v[200:201]
	s_lshl_b32 s0, s75, 8
	v_lshl_add_u64 v[4:5], s[36:37], 0, v[4:5]
	s_ashr_i32 s1, s0, 31
	v_lshl_add_u64 v[4:5], s[0:1], 1, v[4:5]
	v_lshl_add_u64 v[4:5], v[4:5], 0, s[76:77]
	v_pk_mul_f32 v[8:9], v[198:199], v[164:165] op_sel_hi:[0,1]
	v_pk_mul_f32 v[6:7], v[198:199], v[162:163] op_sel_hi:[0,1]
	v_pk_mul_f32 v[10:11], v[198:199], v[160:161] op_sel_hi:[0,1]
	v_pk_mul_f32 v[12:13], v[198:199], v[158:159] op_sel_hi:[0,1]
	v_lshl_add_u64 v[4:5], v[4:5], 0, v[2:3]
	v_cvt_pk_bf16_f32 v6, v6, v7
	v_cvt_pk_bf16_f32 v7, v8, v9
	v_cvt_pk_bf16_f32 v8, v12, v13
	v_cvt_pk_bf16_f32 v9, v10, v11
	s_nop 15
	s_nop 15
	global_store_dwordx4 v[4:5], v[6:9], off
	v_pk_mul_f32 v[10:11], v[198:199], v[144:145] op_sel_hi:[0,1]
	v_pk_mul_f32 v[12:13], v[198:199], v[142:143] op_sel_hi:[0,1]
	v_pk_mul_f32 v[8:9], v[198:199], v[152:153] op_sel_hi:[0,1]
	v_pk_mul_f32 v[6:7], v[198:199], v[150:151] op_sel_hi:[0,1]
	v_cvt_pk_bf16_f32 v6, v6, v7
	v_cvt_pk_bf16_f32 v7, v8, v9
	v_cvt_pk_bf16_f32 v8, v12, v13
	v_cvt_pk_bf16_f32 v9, v10, v11
	global_store_dwordx4 v[4:5], v[6:9], off offset:256
	v_pk_mul_f32 v[10:11], v[196:197], v[148:149] op_sel_hi:[0,1]
	v_pk_mul_f32 v[12:13], v[196:197], v[146:147] op_sel_hi:[0,1]
	v_pk_mul_f32 v[8:9], v[196:197], v[156:157] op_sel_hi:[0,1]
	v_pk_mul_f32 v[6:7], v[196:197], v[154:155] op_sel_hi:[0,1]
	v_cvt_pk_bf16_f32 v6, v6, v7
	v_cvt_pk_bf16_f32 v7, v8, v9
	v_cvt_pk_bf16_f32 v9, v10, v11
	v_add_co_u32_e32 v10, vcc, s31, v4
	v_cvt_pk_bf16_f32 v8, v12, v13
	s_nop 0
	v_addc_co_u32_e32 v11, vcc, 0, v5, vcc
	global_store_dwordx4 v[10:11], v[6:9], off
	v_pk_mul_f32 v[12:13], v[196:197], v[128:129] op_sel_hi:[0,1]
	v_pk_mul_f32 v[14:15], v[196:197], v[126:127] op_sel_hi:[0,1]
	v_pk_mul_f32 v[8:9], v[196:197], v[136:137] op_sel_hi:[0,1]
	v_pk_mul_f32 v[6:7], v[196:197], v[134:135] op_sel_hi:[0,1]
	v_cvt_pk_bf16_f32 v6, v6, v7
	v_cvt_pk_bf16_f32 v7, v8, v9
	v_cvt_pk_bf16_f32 v8, v14, v15
	v_cvt_pk_bf16_f32 v9, v12, v13
	global_store_dwordx4 v[10:11], v[6:9], off offset:256
	v_pk_mul_f32 v[10:11], v[194:195], v[132:133] op_sel_hi:[0,1]
	s_mov_b32 s0, 0x10000
	v_pk_mul_f32 v[8:9], v[194:195], v[140:141] op_sel_hi:[0,1]
	v_pk_mul_f32 v[6:7], v[194:195], v[138:139] op_sel_hi:[0,1]
	v_pk_mul_f32 v[12:13], v[194:195], v[130:131] op_sel_hi:[0,1]
	v_cvt_pk_bf16_f32 v6, v6, v7
	v_cvt_pk_bf16_f32 v7, v8, v9
	v_cvt_pk_bf16_f32 v9, v10, v11
	v_add_co_u32_e32 v10, vcc, s0, v4
	v_cvt_pk_bf16_f32 v8, v12, v13
	s_nop 0
	v_addc_co_u32_e32 v11, vcc, 0, v5, vcc
	global_store_dwordx4 v[10:11], v[6:9], off
	v_pk_mul_f32 v[12:13], v[194:195], v[110:111] op_sel_hi:[0,1]
	v_pk_mul_f32 v[14:15], v[194:195], v[108:109] op_sel_hi:[0,1]
	v_pk_mul_f32 v[8:9], v[194:195], v[120:121] op_sel_hi:[0,1]
	v_pk_mul_f32 v[6:7], v[194:195], v[118:119] op_sel_hi:[0,1]
	v_cvt_pk_bf16_f32 v6, v6, v7
	v_cvt_pk_bf16_f32 v7, v8, v9
	v_cvt_pk_bf16_f32 v8, v14, v15
	v_cvt_pk_bf16_f32 v9, v12, v13
	global_store_dwordx4 v[10:11], v[6:9], off offset:256
	v_pk_mul_f32 v[10:11], v[192:193], v[114:115] op_sel_hi:[0,1]
	s_mov_b32 s0, 0x18000
	v_pk_mul_f32 v[8:9], v[192:193], v[124:125] op_sel_hi:[0,1]
	v_pk_mul_f32 v[6:7], v[192:193], v[122:123] op_sel_hi:[0,1]
	v_pk_mul_f32 v[12:13], v[192:193], v[112:113] op_sel_hi:[0,1]
	v_cvt_pk_bf16_f32 v6, v6, v7
	v_cvt_pk_bf16_f32 v7, v8, v9
	v_cvt_pk_bf16_f32 v9, v10, v11
	v_add_co_u32_e32 v10, vcc, s0, v4
	v_cvt_pk_bf16_f32 v8, v12, v13
	s_nop 0
	v_addc_co_u32_e32 v11, vcc, 0, v5, vcc
	global_store_dwordx4 v[10:11], v[6:9], off
	v_pk_mul_f32 v[12:13], v[192:193], v[102:103] op_sel_hi:[0,1]
	v_pk_mul_f32 v[14:15], v[192:193], v[100:101] op_sel_hi:[0,1]
	v_pk_mul_f32 v[8:9], v[192:193], v[106:107] op_sel_hi:[0,1]
	v_pk_mul_f32 v[6:7], v[192:193], v[104:105] op_sel_hi:[0,1]
	v_cvt_pk_bf16_f32 v6, v6, v7
	v_cvt_pk_bf16_f32 v7, v8, v9
	v_cvt_pk_bf16_f32 v8, v14, v15
	v_cvt_pk_bf16_f32 v9, v12, v13
	global_store_dwordx4 v[10:11], v[6:9], off offset:256
	v_pk_mul_f32 v[10:11], v[190:191], v[94:95] op_sel_hi:[0,1]
	v_pk_mul_f32 v[12:13], v[190:191], v[92:93] op_sel_hi:[0,1]
	v_pk_mul_f32 v[8:9], v[190:191], v[98:99] op_sel_hi:[0,1]
	v_pk_mul_f32 v[6:7], v[190:191], v[96:97] op_sel_hi:[0,1]
	v_cvt_pk_bf16_f32 v6, v6, v7
	v_cvt_pk_bf16_f32 v7, v8, v9
	v_cvt_pk_bf16_f32 v9, v10, v11
	v_add_co_u32_e32 v10, vcc, s16, v4
	v_cvt_pk_bf16_f32 v8, v12, v13
	s_nop 0
	v_addc_co_u32_e32 v11, vcc, 0, v5, vcc
	global_store_dwordx4 v[10:11], v[6:9], off
	v_pk_mul_f32 v[12:13], v[190:191], v[70:71] op_sel_hi:[0,1]
	v_pk_mul_f32 v[14:15], v[190:191], v[68:69] op_sel_hi:[0,1]
	v_pk_mul_f32 v[8:9], v[190:191], v[78:79] op_sel_hi:[0,1]
	v_pk_mul_f32 v[6:7], v[190:191], v[76:77] op_sel_hi:[0,1]
	v_cvt_pk_bf16_f32 v6, v6, v7
	v_cvt_pk_bf16_f32 v7, v8, v9
	v_cvt_pk_bf16_f32 v8, v14, v15
	v_cvt_pk_bf16_f32 v9, v12, v13
	global_store_dwordx4 v[10:11], v[6:9], off offset:256
	v_pk_mul_f32 v[10:11], v[188:189], v[74:75] op_sel_hi:[0,1]
	s_mov_b32 s0, 0x48000
	v_pk_mul_f32 v[8:9], v[188:189], v[82:83] op_sel_hi:[0,1]
	v_pk_mul_f32 v[6:7], v[188:189], v[80:81] op_sel_hi:[0,1]
	v_pk_mul_f32 v[12:13], v[188:189], v[72:73] op_sel_hi:[0,1]
	v_cvt_pk_bf16_f32 v6, v6, v7
	v_cvt_pk_bf16_f32 v7, v8, v9
	v_cvt_pk_bf16_f32 v9, v10, v11
	v_add_co_u32_e32 v10, vcc, s0, v4
	v_cvt_pk_bf16_f32 v8, v12, v13
	s_nop 0
	v_addc_co_u32_e32 v11, vcc, 0, v5, vcc
	global_store_dwordx4 v[10:11], v[6:9], off
	v_pk_mul_f32 v[12:13], v[188:189], v[46:47] op_sel_hi:[0,1]
	v_pk_mul_f32 v[14:15], v[188:189], v[44:45] op_sel_hi:[0,1]
	v_pk_mul_f32 v[8:9], v[188:189], v[54:55] op_sel_hi:[0,1]
	v_pk_mul_f32 v[6:7], v[188:189], v[52:53] op_sel_hi:[0,1]
	v_cvt_pk_bf16_f32 v6, v6, v7
	v_cvt_pk_bf16_f32 v7, v8, v9
	v_cvt_pk_bf16_f32 v8, v14, v15
	v_cvt_pk_bf16_f32 v9, v12, v13
	global_store_dwordx4 v[10:11], v[6:9], off offset:256
	v_pk_mul_f32 v[10:11], v[186:187], v[50:51] op_sel_hi:[0,1]
	s_mov_b32 s0, 0x50000
	v_pk_mul_f32 v[8:9], v[186:187], v[58:59] op_sel_hi:[0,1]
	v_pk_mul_f32 v[6:7], v[186:187], v[56:57] op_sel_hi:[0,1]
	v_pk_mul_f32 v[12:13], v[186:187], v[48:49] op_sel_hi:[0,1]
	v_cvt_pk_bf16_f32 v6, v6, v7
	v_cvt_pk_bf16_f32 v7, v8, v9
	v_cvt_pk_bf16_f32 v9, v10, v11
	v_add_co_u32_e32 v10, vcc, s0, v4
	v_cvt_pk_bf16_f32 v8, v12, v13
	s_nop 0
	v_addc_co_u32_e32 v11, vcc, 0, v5, vcc
	global_store_dwordx4 v[10:11], v[6:9], off
	v_pk_mul_f32 v[12:13], v[186:187], v[86:87] op_sel_hi:[0,1]
	v_pk_mul_f32 v[14:15], v[186:187], v[84:85] op_sel_hi:[0,1]
	v_pk_mul_f32 v[8:9], v[186:187], v[90:91] op_sel_hi:[0,1]
	v_pk_mul_f32 v[6:7], v[186:187], v[88:89] op_sel_hi:[0,1]
	v_cvt_pk_bf16_f32 v6, v6, v7
	v_cvt_pk_bf16_f32 v7, v8, v9
	v_cvt_pk_bf16_f32 v8, v14, v15
	v_cvt_pk_bf16_f32 v9, v12, v13
	global_store_dwordx4 v[10:11], v[6:9], off offset:256
	v_pk_mul_f32 v[10:11], v[184:185], v[38:39] op_sel_hi:[0,1]
	s_mov_b32 s0, 0x58000
	v_pk_mul_f32 v[8:9], v[184:185], v[42:43] op_sel_hi:[0,1]
	v_pk_mul_f32 v[6:7], v[184:185], v[40:41] op_sel_hi:[0,1]
	v_pk_mul_f32 v[12:13], v[184:185], v[36:37] op_sel_hi:[0,1]
	v_cvt_pk_bf16_f32 v6, v6, v7
	v_cvt_pk_bf16_f32 v7, v8, v9
	v_cvt_pk_bf16_f32 v9, v10, v11
	v_add_co_u32_e32 v10, vcc, s0, v4
	v_cvt_pk_bf16_f32 v8, v12, v13
	s_nop 0
	v_addc_co_u32_e32 v11, vcc, 0, v5, vcc
	global_store_dwordx4 v[10:11], v[6:9], off
	v_pk_mul_f32 v[4:5], v[184:185], v[64:65] op_sel_hi:[0,1]
	v_pk_mul_f32 v[12:13], v[184:185], v[60:61] op_sel_hi:[0,1]
	v_pk_mul_f32 v[6:7], v[184:185], v[66:67] op_sel_hi:[0,1]
	v_pk_mul_f32 v[8:9], v[184:185], v[62:63] op_sel_hi:[0,1]
	v_cvt_pk_bf16_f32 v4, v4, v5
	v_cvt_pk_bf16_f32 v5, v6, v7
	v_cvt_pk_bf16_f32 v6, v12, v13
	v_cvt_pk_bf16_f32 v7, v8, v9
	s_and_b64 vcc, exec, s[38:39]
	s_mov_b32 s75, s48
	s_mov_b32 s58, s46
	s_mov_b64 s[56:57], s[52:53]
	s_mov_b64 s[54:55], s[50:51]
	global_store_dwordx4 v[10:11], v[4:7], off offset:256
	s_cbranch_vccz .LBB0_1981
	s_waitcnt vmcnt(0)
	s_cmpk_gt_u32 s21, 0xff
	s_movk_i32 s74, 0x1ff
	s_cbranch_scc1 .LBB0_1988
	s_barrier

.Lpeelqc_hdr:
	s_add_u32 s40, s42, 0x100
	s_addc_u32 s41, s43, 0
	s_cmp_eq_u32 s76, 4
	s_cselect_b32 s59, s55, s41
	s_cselect_b32 s58, s54, s40
	s_cselect_b32 s45, s57, s1
	s_cselect_b32 s44, s56, s0
	s_add_i32 s78, 0, 0x10400
	v_add_u32_e32 v2, s78, v214
	ds_read_b128 v[12:15], v2
	ds_read_b128 v[16:19], v2 offset:1024
	ds_read_b128 v[4:7], v2 offset:2048
	ds_read_b128 v[8:11], v2 offset:3072
	v_lshl_add_u64 v[20:21], s[42:43], 0, v[204:205]
	s_add_i32 m0, s64, 0xc400
	ds_read_b128 v[170:173], v216 offset:1024
	ds_read_b128 v[174:177], v216 offset:2048
	ds_read_b128 v[218:221], v216 offset:3072
	ds_read_b128 v[222:225], v216 offset:4096
	ds_read_b128 v[230:233], v216 offset:5120
	ds_read_b128 v[234:237], v216 offset:6144
	ds_read_b128 v[240:243], v216 offset:7168
	ds_read_b128 v[244:247], v216 offset:8192
	global_load_lds_dwordx4 v[20:21], off
	v_lshl_add_u64 v[20:21], s[42:43], 0, v[202:203]
	s_add_i32 m0, s64, 0xe400
	s_nop 0
	global_load_lds_dwordx4 v[20:21], off
	s_waitcnt lgkmcnt(8)
	s_barrier
	s_waitcnt lgkmcnt(0)
	s_setprio 1
	s_waitcnt lgkmcnt(0)
	v_mfma_scale_f32_16x16x128_f8f6f4 v[162:165], v[12:19], v[170:177], 0, v117, v212 op_sel_hi:[0,0,0]
	v_mfma_scale_f32_16x16x128_f8f6f4 v[154:157], v[4:11], v[170:177], 0, v117, v212 op_sel_hi:[0,0,0]
	v_mfma_scale_f32_16x16x128_f8f6f4 v[146:149], v[12:19], v[218:225], 0, v117, v212 op_sel_hi:[0,0,0]
	v_mfma_scale_f32_16x16x128_f8f6f4 v[138:141], v[4:11], v[218:225], 0, v117, v212 op_sel_hi:[0,0,0]
	v_mfma_scale_f32_16x16x128_f8f6f4 v[130:133], v[12:19], v[230:237], 0, v117, v212 op_sel_hi:[0,0,0]
	v_mfma_scale_f32_16x16x128_f8f6f4 v[122:125], v[4:11], v[230:237], 0, v117, v212 op_sel_hi:[0,0,0]
	v_mfma_scale_f32_16x16x128_f8f6f4 v[112:115], v[12:19], v[240:247], 0, v117, v212 op_sel_hi:[0,0,0]
	v_mfma_scale_f32_16x16x128_f8f6f4 v[104:107], v[4:11], v[240:247], 0, v117, v212 op_sel_hi:[0,0,0]
	s_setprio 0
	s_barrier
	s_add_i32 s42, 0, 0x14400
	s_add_i32 s43, s78, s61
	v_add_u32_e32 v2, s42, v214
	v_lshl_add_u64 v[166:167], s[44:45], 0, v[184:185]
	s_mov_b32 m0, s43
	ds_read_b128 v[28:31], v2
	ds_read_b128 v[32:35], v2 offset:1024
	ds_read_b128 v[20:23], v2 offset:2048
	ds_read_b128 v[24:27], v2 offset:3072
	global_load_lds_dwordx4 v[166:167], off
	v_lshl_add_u64 v[168:169], s[44:45], 0, v[186:187]
	s_add_i32 m0, s43, 0x2000
	s_nop 0
	global_load_lds_dwordx4 v[168:169], off
	s_barrier
	s_waitcnt lgkmcnt(0)
	s_setprio 1
	s_waitcnt lgkmcnt(0)
	v_mfma_scale_f32_16x16x128_f8f6f4 v[158:161], v[28:35], v[170:177], 0, v117, v212 op_sel_hi:[0,0,0]
	v_mfma_scale_f32_16x16x128_f8f6f4 v[150:153], v[20:27], v[170:177], 0, v117, v212 op_sel_hi:[0,0,0]
	v_mfma_scale_f32_16x16x128_f8f6f4 v[142:145], v[28:35], v[218:225], 0, v117, v212 op_sel_hi:[0,0,0]
	v_mfma_scale_f32_16x16x128_f8f6f4 v[134:137], v[20:27], v[218:225], 0, v117, v212 op_sel_hi:[0,0,0]
	v_mfma_scale_f32_16x16x128_f8f6f4 v[126:129], v[28:35], v[230:237], 0, v117, v212 op_sel_hi:[0,0,0]
	v_mfma_scale_f32_16x16x128_f8f6f4 v[118:121], v[20:27], v[230:237], 0, v117, v212 op_sel_hi:[0,0,0]
	v_mfma_scale_f32_16x16x128_f8f6f4 v[108:111], v[28:35], v[240:247], 0, v117, v212 op_sel_hi:[0,0,0]
	v_mfma_scale_f32_16x16x128_f8f6f4 v[100:103], v[20:27], v[240:247], 0, v117, v212 op_sel_hi:[0,0,0]
	s_setprio 0
	s_mov_b32 m0, s65
	v_lshl_add_u64 v[170:171], s[58:59], 0, v[188:189]
	s_barrier
	ds_read_b128 v[174:177], v216 offset:17408
	ds_read_b128 v[178:181], v216 offset:18432
	ds_read_b128 v[218:221], v216 offset:19456
	ds_read_b128 v[222:225], v216 offset:20480
	ds_read_b128 v[230:233], v216 offset:21504
	ds_read_b128 v[234:237], v216 offset:22528
	ds_read_b128 v[240:243], v216 offset:23552
	ds_read_b128 v[244:247], v216 offset:24576
	global_load_lds_dwordx4 v[170:171], off
	v_lshl_add_u64 v[172:173], s[58:59], 0, v[190:191]
	s_mov_b32 m0, s66
	s_nop 0
	global_load_lds_dwordx4 v[172:173], off
	s_barrier
	s_waitcnt lgkmcnt(0)
	s_setprio 1
	s_waitcnt lgkmcnt(0)
	v_mfma_scale_f32_16x16x128_f8f6f4 v[96:99], v[12:19], v[174:181], 0, v117, v212 op_sel_hi:[0,0,0]
	v_mfma_scale_f32_16x16x128_f8f6f4 v[88:91], v[4:11], v[174:181], 0, v117, v212 op_sel_hi:[0,0,0]
	v_mfma_scale_f32_16x16x128_f8f6f4 v[80:83], v[12:19], v[218:225], 0, v117, v212 op_sel_hi:[0,0,0]
	v_mfma_scale_f32_16x16x128_f8f6f4 v[72:75], v[4:11], v[218:225], 0, v117, v212 op_sel_hi:[0,0,0]
	v_mfma_scale_f32_16x16x128_f8f6f4 v[60:63], v[12:19], v[230:237], 0, v117, v212 op_sel_hi:[0,0,0]
	v_mfma_scale_f32_16x16x128_f8f6f4 v[48:51], v[4:11], v[230:237], 0, v117, v212 op_sel_hi:[0,0,0]
	v_mfma_scale_f32_16x16x128_f8f6f4 v[40:43], v[12:19], v[240:247], 0, v117, v212 op_sel_hi:[0,0,0]
	v_mfma_scale_f32_16x16x128_f8f6f4 v[36:39], v[4:11], v[240:247], 0, v117, v212 op_sel_hi:[0,0,0]
	s_setprio 0
	s_barrier
	s_add_u32 s78, s44, 0x20000
	s_addc_u32 s79, s45, 0
	s_add_i32 s42, s42, s61
	v_lshl_add_u64 v[4:5], s[78:79], 0, v[184:185]
	s_mov_b32 m0, s42
	s_nop 0
	global_load_lds_dwordx4 v[4:5], off
	v_lshl_add_u64 v[4:5], s[78:79], 0, v[186:187]
	s_add_i32 m0, s42, 0x2000
	s_nop 0
	global_load_lds_dwordx4 v[4:5], off
	s_waitcnt vmcnt(6)
	s_barrier
	s_setprio 1
	v_mfma_scale_f32_16x16x128_f8f6f4 v[92:95], v[28:35], v[174:181], 0, v117, v212 op_sel_hi:[0,0,0]
	v_mfma_scale_f32_16x16x128_f8f6f4 v[84:87], v[20:27], v[174:181], 0, v117, v212 op_sel_hi:[0,0,0]
	v_mfma_scale_f32_16x16x128_f8f6f4 v[76:79], v[28:35], v[218:225], 0, v117, v212 op_sel_hi:[0,0,0]
	v_mfma_scale_f32_16x16x128_f8f6f4 v[64:67], v[20:27], v[218:225], 0, v117, v212 op_sel_hi:[0,0,0]
	v_mfma_scale_f32_16x16x128_f8f6f4 v[68:71], v[28:35], v[230:237], 0, v117, v212 op_sel_hi:[0,0,0]
	v_mfma_scale_f32_16x16x128_f8f6f4 v[56:59], v[20:27], v[230:237], 0, v117, v212 op_sel_hi:[0,0,0]
	v_mfma_scale_f32_16x16x128_f8f6f4 v[52:55], v[28:35], v[240:247], 0, v117, v212 op_sel_hi:[0,0,0]
	v_mfma_scale_f32_16x16x128_f8f6f4 v[44:47], v[20:27], v[240:247], 0, v117, v212 op_sel_hi:[0,0,0]
	s_setprio 0
	s_add_i32 s42, 0, 0x18400
	v_add_u32_e32 v2, s42, v214
	s_barrier
	ds_read_b128 v[12:15], v2
	ds_read_b128 v[16:19], v2 offset:1024
	ds_read_b128 v[4:7], v2 offset:2048
	ds_read_b128 v[8:11], v2 offset:3072
	s_mov_b32 m0, s67
	v_lshl_add_u64 v[182:183], s[58:59], 0, v[192:193]
	ds_read_b128 v[20:23], v216 offset:33792
	ds_read_b128 v[24:27], v216 offset:34816
	ds_read_b128 v[28:31], v216 offset:35840
	ds_read_b128 v[32:35], v216 offset:36864
	ds_read_b128 v[174:177], v216 offset:37888
	ds_read_b128 v[178:181], v216 offset:38912
	ds_read_b128 v[218:221], v216 offset:39936
	ds_read_b128 v[222:225], v216 offset:40960
	global_load_lds_dwordx4 v[182:183], off
	v_lshl_add_u64 v[182:183], s[58:59], 0, v[194:195]
	s_mov_b32 m0, s68
	s_nop 0
	global_load_lds_dwordx4 v[182:183], off
	s_waitcnt lgkmcnt(8)
	s_barrier
	s_waitcnt lgkmcnt(0)
	s_setprio 1
	s_waitcnt lgkmcnt(0)
	v_mfma_scale_f32_16x16x128_f8f6f4 v[162:165], v[12:19], v[20:27], v[162:165], v117, v212 op_sel_hi:[0,0,0]
	v_mfma_scale_f32_16x16x128_f8f6f4 v[154:157], v[4:11], v[20:27], v[154:157], v117, v212 op_sel_hi:[0,0,0]
	v_mfma_scale_f32_16x16x128_f8f6f4 v[146:149], v[12:19], v[28:35], v[146:149], v117, v212 op_sel_hi:[0,0,0]
	v_mfma_scale_f32_16x16x128_f8f6f4 v[138:141], v[4:11], v[28:35], v[138:141], v117, v212 op_sel_hi:[0,0,0]
	v_mfma_scale_f32_16x16x128_f8f6f4 v[130:133], v[12:19], v[174:181], v[130:133], v117, v212 op_sel_hi:[0,0,0]
	v_mfma_scale_f32_16x16x128_f8f6f4 v[122:125], v[4:11], v[174:181], v[122:125], v117, v212 op_sel_hi:[0,0,0]
	v_mfma_scale_f32_16x16x128_f8f6f4 v[112:115], v[12:19], v[218:225], v[112:115], v117, v212 op_sel_hi:[0,0,0]
	v_mfma_scale_f32_16x16x128_f8f6f4 v[104:107], v[4:11], v[218:225], v[104:107], v117, v212 op_sel_hi:[0,0,0]
	s_setprio 0
	s_barrier
	s_add_i32 s58, 0, 0x1c400
	s_add_i32 s42, s42, s61
	v_add_u32_e32 v2, s58, v214
	v_lshl_add_u64 v[166:167], v[166:167], 0, s[22:23]
	s_mov_b32 m0, s42
	ds_read_b128 v[230:233], v2
	ds_read_b128 v[234:237], v2 offset:1024
	ds_read_b128 v[240:243], v2 offset:2048
	ds_read_b128 v[244:247], v2 offset:3072
	global_load_lds_dwordx4 v[166:167], off
	v_lshl_add_u64 v[166:167], v[168:169], 0, s[22:23]
	s_add_i32 m0, s42, 0x2000
	s_nop 0
	global_load_lds_dwordx4 v[166:167], off
	s_barrier
	s_waitcnt lgkmcnt(0)
	s_setprio 1
	s_waitcnt lgkmcnt(0)
	v_mfma_scale_f32_16x16x128_f8f6f4 v[158:161], v[230:237], v[20:27], v[158:161], v117, v212 op_sel_hi:[0,0,0]
	v_mfma_scale_f32_16x16x128_f8f6f4 v[150:153], v[240:247], v[20:27], v[150:153], v117, v212 op_sel_hi:[0,0,0]
	v_mfma_scale_f32_16x16x128_f8f6f4 v[142:145], v[230:237], v[28:35], v[142:145], v117, v212 op_sel_hi:[0,0,0]
	v_mfma_scale_f32_16x16x128_f8f6f4 v[134:137], v[240:247], v[28:35], v[134:137], v117, v212 op_sel_hi:[0,0,0]
	v_mfma_scale_f32_16x16x128_f8f6f4 v[126:129], v[230:237], v[174:181], v[126:129], v117, v212 op_sel_hi:[0,0,0]
	v_mfma_scale_f32_16x16x128_f8f6f4 v[118:121], v[240:247], v[174:181], v[118:121], v117, v212 op_sel_hi:[0,0,0]
	v_mfma_scale_f32_16x16x128_f8f6f4 v[108:111], v[230:237], v[218:225], v[108:111], v117, v212 op_sel_hi:[0,0,0]
	v_mfma_scale_f32_16x16x128_f8f6f4 v[100:103], v[240:247], v[218:225], v[100:103], v117, v212 op_sel_hi:[0,0,0]
	s_setprio 0
	s_mov_b32 m0, s71
	v_lshl_add_u64 v[166:167], v[170:171], 0, s[22:23]
	s_barrier
	ds_read_b128 v[20:23], v216 offset:50176
	ds_read_b128 v[24:27], v216 offset:51200
	ds_read_b128 v[28:31], v216 offset:52224
	ds_read_b128 v[32:35], v216 offset:53248
	ds_read_b128 v[174:177], v216 offset:54272
	ds_read_b128 v[178:181], v216 offset:55296
	ds_read_b128 v[218:221], v216 offset:56320
	ds_read_b128 v[222:225], v216 offset:57344
	global_load_lds_dwordx4 v[166:167], off
	v_lshl_add_u64 v[166:167], v[172:173], 0, s[22:23]
	s_mov_b32 m0, s72
	s_nop 0
	global_load_lds_dwordx4 v[166:167], off
	s_barrier
	s_waitcnt lgkmcnt(0)
	s_setprio 1
	s_waitcnt lgkmcnt(0)
	v_mfma_scale_f32_16x16x128_f8f6f4 v[96:99], v[12:19], v[20:27], v[96:99], v117, v212 op_sel_hi:[0,0,0]
	v_mfma_scale_f32_16x16x128_f8f6f4 v[88:91], v[4:11], v[20:27], v[88:91], v117, v212 op_sel_hi:[0,0,0]
	v_mfma_scale_f32_16x16x128_f8f6f4 v[80:83], v[12:19], v[28:35], v[80:83], v117, v212 op_sel_hi:[0,0,0]
	v_mfma_scale_f32_16x16x128_f8f6f4 v[72:75], v[4:11], v[28:35], v[72:75], v117, v212 op_sel_hi:[0,0,0]
	v_mfma_scale_f32_16x16x128_f8f6f4 v[60:63], v[12:19], v[174:181], v[60:63], v117, v212 op_sel_hi:[0,0,0]
	v_mfma_scale_f32_16x16x128_f8f6f4 v[48:51], v[4:11], v[174:181], v[48:51], v117, v212 op_sel_hi:[0,0,0]
	v_mfma_scale_f32_16x16x128_f8f6f4 v[40:43], v[12:19], v[218:225], v[40:43], v117, v212 op_sel_hi:[0,0,0]
	v_mfma_scale_f32_16x16x128_f8f6f4 v[36:39], v[4:11], v[218:225], v[36:39], v117, v212 op_sel_hi:[0,0,0]
	s_setprio 0
	s_barrier
	s_add_u32 s42, s44, 0x20080
	s_addc_u32 s43, s45, 0
	s_add_i32 s44, s58, s61
	v_lshl_add_u64 v[4:5], s[42:43], 0, v[184:185]
	s_mov_b32 m0, s44
	s_nop 0
	global_load_lds_dwordx4 v[4:5], off
	v_lshl_add_u64 v[4:5], s[42:43], 0, v[186:187]
	s_add_i32 m0, s44, 0x2000
	s_nop 0
	global_load_lds_dwordx4 v[4:5], off
	s_waitcnt vmcnt(6)
	s_barrier
	s_setprio 1
	v_mfma_scale_f32_16x16x128_f8f6f4 v[92:95], v[230:237], v[20:27], v[92:95], v117, v212 op_sel_hi:[0,0,0]
	v_mfma_scale_f32_16x16x128_f8f6f4 v[84:87], v[240:247], v[20:27], v[84:87], v117, v212 op_sel_hi:[0,0,0]
	v_mfma_scale_f32_16x16x128_f8f6f4 v[76:79], v[230:237], v[28:35], v[76:79], v117, v212 op_sel_hi:[0,0,0]
	v_mfma_scale_f32_16x16x128_f8f6f4 v[64:67], v[240:247], v[28:35], v[64:67], v117, v212 op_sel_hi:[0,0,0]
	v_mfma_scale_f32_16x16x128_f8f6f4 v[68:71], v[230:237], v[174:181], v[68:71], v117, v212 op_sel_hi:[0,0,0]
	v_mfma_scale_f32_16x16x128_f8f6f4 v[56:59], v[240:247], v[174:181], v[56:59], v117, v212 op_sel_hi:[0,0,0]
	v_mfma_scale_f32_16x16x128_f8f6f4 v[52:55], v[230:237], v[218:225], v[52:55], v117, v212 op_sel_hi:[0,0,0]
	v_mfma_scale_f32_16x16x128_f8f6f4 v[44:47], v[240:247], v[218:225], v[44:47], v117, v212 op_sel_hi:[0,0,0]
	s_setprio 0
	s_add_i32 s76, s76, 2
	s_add_u32 s0, s0, 0x100
	s_addc_u32 s1, s1, 0
	s_cmp_gt_u32 s76, 5
	s_mov_b64 s[42:43], s[40:41]
	s_barrier
	s_cbranch_scc0 .LBB0_2034
	s_branch .Lpexit_qc
